# P10 query tile stores and the P12 unnormalised output pieces with nt policy
# baseline (speedup 1.0000x reference)
; __device__ __forceinline__ int fresh_lane() { int l; asm volatile("v_mbcnt_lo_u32_b32 %0, -1, 0\n\tv_mbcnt_hi_u32_b32 %0, -1, %0" : "=v"(l)); return l; }
; __device__ __forceinline__ unsigned cvt_pk_bf16(float lo, float hi) { unsigned r; asm volatile("v_cvt_pk_bf16_f32 %0, %1, %2" : "=v"(r) : "v"(lo), "v"(hi)); return r; }
;     __device__ __forceinline__ void operator()(const f32x4 (&acc)[2][2][4][2], const Unit& u, int wr, int wc, int fr_, int fq_) const {
;         const int l_ = fresh_lane(), fr = l_ & 15, fq = l_ >> 4;
;         const int row0 = u.pm * BM + wr * 64 + fr, col0 = u.pn * BM + wc * 32 + 8 * fq;
; #pragma unroll
;         for (int ai = 0; ai < 2; ++ai)
; #pragma unroll
;             for (int m = 0; m < 4; ++m) { bf16_t* rowp = O + (size_t)(row0 + ai * HALF + m * 16) * ldc + col0;
; #pragma unroll
;                 for (int bj = 0; bj < 2; ++bj) { const f32x4 v0 = acc[ai][bj][m][0], v1 = acc[ai][bj][m][1];
;                     u32x4 w; w.x = cvt_pk_bf16(v0[0], v0[1]); w.y = cvt_pk_bf16(v0[2], v0[3]); w.z = cvt_pk_bf16(v1[0], v1[1]); w.w = cvt_pk_bf16(v1[2], v1[3]);
;                     *(u32x4*)(rowp + bj * HALF) = w; } }
.LBB0_3154:
	s_lshl_b32 s39, s46, 8
	v_mbcnt_lo_u32_b32 v140, -1, 0
	v_mbcnt_hi_u32_b32 v140, -1, v140
	s_add_i32 s39, s39, s62
	v_and_or_b32 v146, v140, 15, s39
	s_lshl_b32 s39, s74, 8
	v_ashrrev_i32_e32 v140, 1, v140
	s_or_b32 s39, s39, s63
	v_and_b32_e32 v140, -8, v140
	v_add_u32_e32 v140, s39, v140
	v_ashrrev_i32_e32 v147, 31, v146
	v_ashrrev_i32_e32 v141, 31, v140
	v_lshlrev_b64 v[148:149], 12, v[146:147]
	v_lshl_add_u64 v[148:149], s[12:13], 0, v[148:149]
	v_lshlrev_b64 v[150:151], 1, v[140:141]
	v_lshl_add_u64 v[140:141], v[148:149], 0, v[150:151]
	v_cvt_pk_bf16_f32 v126, v126, v127
	v_cvt_pk_bf16_f32 v127, v128, v129
	v_cvt_pk_bf16_f32 v128, v122, v123
	v_cvt_pk_bf16_f32 v129, v124, v125
	global_store_dwordx4 v[140:141], v[126:129], off nt
	v_cvt_pk_bf16_f32 v114, v114, v115
	v_cvt_pk_bf16_f32 v115, v116, v117
	v_cvt_pk_bf16_f32 v116, v106, v107
	v_or_b32_e32 v106, 16, v146
	v_ashrrev_i32_e32 v107, 31, v106
	v_lshlrev_b64 v[106:107], 12, v[106:107]
	v_lshl_add_u64 v[106:107], s[12:13], 0, v[106:107]
	v_cvt_pk_bf16_f32 v117, v108, v109
	global_store_dwordx4 v[140:141], v[114:117], off offset:256 nt
	s_nop 1
	v_lshl_add_u64 v[114:115], v[106:107], 0, v[150:151]
	v_cvt_pk_bf16_f32 v106, v118, v119
	v_cvt_pk_bf16_f32 v107, v120, v121
	v_cvt_pk_bf16_f32 v108, v110, v111
	v_cvt_pk_bf16_f32 v109, v112, v113
	global_store_dwordx4 v[114:115], v[106:109], off nt
	v_cvt_pk_bf16_f32 v98, v98, v99
	v_cvt_pk_bf16_f32 v99, v100, v101
	v_cvt_pk_bf16_f32 v100, v90, v91
	v_or_b32_e32 v90, 32, v146
	v_ashrrev_i32_e32 v91, 31, v90
	v_lshlrev_b64 v[90:91], 12, v[90:91]
	v_lshl_add_u64 v[90:91], s[12:13], 0, v[90:91]
	v_cvt_pk_bf16_f32 v101, v92, v93
	global_store_dwordx4 v[114:115], v[98:101], off offset:256 nt
	s_nop 1
	v_lshl_add_u64 v[98:99], v[90:91], 0, v[150:151]
	v_cvt_pk_bf16_f32 v90, v102, v103
	v_cvt_pk_bf16_f32 v91, v104, v105
	v_cvt_pk_bf16_f32 v92, v94, v95
	v_cvt_pk_bf16_f32 v93, v96, v97
	global_store_dwordx4 v[98:99], v[90:93], off nt
	v_cvt_pk_bf16_f32 v82, v82, v83
	v_cvt_pk_bf16_f32 v83, v84, v85
	v_cvt_pk_bf16_f32 v84, v74, v75
	v_or_b32_e32 v74, 48, v146
	v_ashrrev_i32_e32 v75, 31, v74
	v_lshlrev_b64 v[74:75], 12, v[74:75]
	v_lshl_add_u64 v[74:75], s[12:13], 0, v[74:75]
	v_cvt_pk_bf16_f32 v85, v76, v77
	global_store_dwordx4 v[98:99], v[82:85], off offset:256 nt
	s_nop 1
	v_lshl_add_u64 v[82:83], v[74:75], 0, v[150:151]
	v_cvt_pk_bf16_f32 v74, v86, v87
	v_cvt_pk_bf16_f32 v75, v88, v89
	v_cvt_pk_bf16_f32 v76, v78, v79
	v_cvt_pk_bf16_f32 v77, v80, v81
	global_store_dwordx4 v[82:83], v[74:77], off nt
	v_cvt_pk_bf16_f32 v70, v70, v71
	v_cvt_pk_bf16_f32 v71, v72, v73
	v_cvt_pk_bf16_f32 v72, v66, v67
	v_cvt_pk_bf16_f32 v73, v68, v69
	global_store_dwordx4 v[82:83], v[70:73], off offset:256 nt
	v_cvt_pk_bf16_f32 v62, v62, v63
	v_cvt_pk_bf16_f32 v63, v64, v65
	v_cvt_pk_bf16_f32 v64, v58, v59
	v_add_co_u32_e32 v58, vcc, s66, v140
	v_lshl_add_u64 v[66:67], v[140:141], 0, s[4:5]
	s_nop 0
	v_addc_co_u32_e32 v59, vcc, 0, v141, vcc
	v_cvt_pk_bf16_f32 v65, v60, v61
	global_store_dwordx4 v[58:59], v[62:65], off nt
	v_cvt_pk_bf16_f32 v50, v50, v51
	v_cvt_pk_bf16_f32 v51, v52, v53
	v_cvt_pk_bf16_f32 v52, v42, v43
	v_cvt_pk_bf16_f32 v53, v44, v45
	global_store_dwordx4 v[66:67], v[50:53], off offset:256 nt
	v_cvt_pk_bf16_f32 v42, v54, v55
	v_cvt_pk_bf16_f32 v43, v56, v57
	v_cvt_pk_bf16_f32 v44, v46, v47
	v_add_co_u32_e32 v46, vcc, s67, v140
	s_nop 0
	v_lshl_add_u64 v[50:51], v[140:141], 0, s[28:29]
	v_addc_co_u32_e32 v47, vcc, 0, v141, vcc
	v_cvt_pk_bf16_f32 v45, v48, v49
	global_store_dwordx4 v[46:47], v[42:45], off nt
	v_cvt_pk_bf16_f32 v34, v34, v35
	v_cvt_pk_bf16_f32 v35, v36, v37
	v_cvt_pk_bf16_f32 v36, v26, v27
	v_cvt_pk_bf16_f32 v37, v28, v29
	global_store_dwordx4 v[50:51], v[34:37], off offset:256 nt
	v_cvt_pk_bf16_f32 v26, v38, v39
	v_cvt_pk_bf16_f32 v27, v40, v41
	v_cvt_pk_bf16_f32 v28, v30, v31
	v_add_co_u32_e32 v30, vcc, s70, v140
	s_nop 0
	v_lshl_add_u64 v[34:35], v[140:141], 0, s[30:31]
	v_addc_co_u32_e32 v31, vcc, 0, v141, vcc
	v_cvt_pk_bf16_f32 v29, v32, v33
	global_store_dwordx4 v[30:31], v[26:29], off nt
	v_cvt_pk_bf16_f32 v18, v18, v19
	v_cvt_pk_bf16_f32 v19, v20, v21
	v_cvt_pk_bf16_f32 v20, v10, v11
	v_cvt_pk_bf16_f32 v21, v12, v13
	global_store_dwordx4 v[34:35], v[18:21], off offset:256 nt
	v_cvt_pk_bf16_f32 v10, v22, v23
	v_cvt_pk_bf16_f32 v11, v24, v25
	v_cvt_pk_bf16_f32 v12, v14, v15
	v_add_co_u32_e32 v14, vcc, s71, v140
	s_nop 0
	v_lshl_add_u64 v[18:19], v[140:141], 0, s[36:37]
	v_addc_co_u32_e32 v15, vcc, 0, v141, vcc
	s_andn2_b64 vcc, exec, s[0:1]
	s_mov_b64 s[0:1], -1
	v_cvt_pk_bf16_f32 v13, v16, v17
	global_store_dwordx4 v[14:15], v[10:13], off nt
	v_cvt_pk_bf16_f32 v6, v6, v7
	v_cvt_pk_bf16_f32 v7, v8, v9
	v_cvt_pk_bf16_f32 v8, v2, v3
	v_cvt_pk_bf16_f32 v9, v4, v5
	global_store_dwordx4 v[18:19], v[6:9], off offset:256 nt
	s_cbranch_vccnz .LBB0_3143
	s_andn2_b64 vcc, exec, s[10:11]
	s_cbranch_vccnz .LBB0_3142
	s_barrier
	s_branch .LBB0_3142

; #define P12_VISSUE(c_, i_, q_, D_X) do { _Pragma("unroll") for (int b = 0; b < 8; ++b) { const int idx = ((q_) * 8 + b) * 4 + eg; const unsigned ro = (unsigned)(c_) * 16384u + (unsigned)EL[(i_) * 128 + idx]; \
;           const v3u_ ld_ = *(const v3u_*)(V8 + (size_t)(ro * 192u + 12u * (unsigned)cl)); if (b & 1) D_X[b >> 1].hi = ld_; else D_X[b >> 1].lo = ld_; } } while (0)
; __device__ __forceinline__ void p12_peer(Frame& F) {
;     ...
;       for (int c = 0; c < 16; ++c) {
;           int lo_ = 16 * cl + 4 * eg; asm volatile("" : "+v"(lo_));
; _Pragma("nounroll")
;           for (int i = 0; i < 4; ++i) { const int t = F.gw + i * F.NGW;
;               f32x2 acc2[8];
; #pragma unroll
;               for (int m = 0; m < 8; ++m) acc2[m] = (f32x2){0.f, 0.f};
;               const v2u hb = *(const v2u*)(HN + ((size_t)t * D_ + (size_t)(unsigned)(256 * c + lo_)));
;               P12_VISSUE(c, i, 1, dB); asm volatile("" ::: "memory"); P12_VCOMP(i, 0, dA);
;               P12_VISSUE(c, i, 2, dA); asm volatile("" ::: "memory"); P12_VCOMP(i, 1, dB);
;               P12_VISSUE(c, i, 3, dB); asm volatile("" ::: "memory"); P12_VCOMP(i, 2, dA);
;               { const int in_ = i + 1 < 4 ? i + 1 : 0, cn_ = i + 1 < 4 ? c : (c + 1 < 16 ? c + 1 : 15); P12_VISSUE(cn_, in_, 0, dA); } asm volatile("" ::: "memory"); P12_VCOMP(i, 3, dB);
.LBB0_3403:
	v_add_u32_e32 v152, s28, v175
	ds_read_u16 v2, v152
	ds_read_u16 v3, v152 offset:8
	ds_read_u16 v4, v152 offset:16
	ds_read_u16 v5, v152 offset:24
	ds_read_u16 v6, v152 offset:32
	ds_read_u16 v7, v152 offset:40
	ds_read_u16 v8, v152 offset:48
	ds_read_u16 v9, v152 offset:56
	s_ashr_i32 s13, s12, 31
	s_lshl_b64 s[14:15], s[12:13], 13
	v_lshl_add_u64 v[0:1], v[164:165], 0, s[14:15]
	s_cmpk_eq_i32 s28, 0x300
	global_load_dwordx2 v[158:159], v[0:1], off
	s_cselect_b32 s30, 0, s23
	s_waitcnt lgkmcnt(7)
	v_add_u32_e32 v0, s21, v2
	v_lshl_add_u32 v179, s30, 1, v161
	s_waitcnt lgkmcnt(6)
	v_add_u32_e32 v2, s21, v3
	s_waitcnt lgkmcnt(5)
	v_add_u32_e32 v4, s21, v4
	s_waitcnt lgkmcnt(4)
	v_add_u32_e32 v10, s21, v5
	s_waitcnt lgkmcnt(3)
	v_add_u32_e32 v11, s21, v6
	s_waitcnt lgkmcnt(2)
	v_add_u32_e32 v12, s21, v7
	s_waitcnt lgkmcnt(1)
	v_add_u32_e32 v13, s21, v8
	s_waitcnt lgkmcnt(0)
	v_add_u32_e32 v14, s21, v9
	v_mad_u64_u32 v[0:1], s[30:31], v0, s16, v[160:161]
	v_mad_u64_u32 v[2:3], s[30:31], v2, s16, v[160:161]
	v_mad_u64_u32 v[4:5], s[30:31], v4, s16, v[160:161]
	v_mad_u64_u32 v[6:7], s[30:31], v10, s16, v[160:161]
	v_mad_u64_u32 v[8:9], s[30:31], v11, s16, v[160:161]
	v_mad_u64_u32 v[10:11], s[30:31], v12, s16, v[160:161]
	v_mad_u64_u32 v[12:13], s[30:31], v13, s16, v[160:161]
	v_mad_u64_u32 v[14:15], s[30:31], v14, s16, v[160:161]
	global_load_dwordx3 v[154:156], v0, s[2:3]
	global_load_dwordx3 v[220:222], v2, s[2:3]
	global_load_dwordx3 v[180:182], v4, s[2:3]
	global_load_dwordx3 v[224:226], v6, s[2:3]
	global_load_dwordx3 v[186:188], v8, s[2:3]
	global_load_dwordx3 v[228:230], v10, s[2:3]
	global_load_dwordx3 v[192:194], v12, s[2:3]
	global_load_dwordx3 v[232:234], v14, s[2:3]
	ds_read2_b32 v[166:167], v177 offset1:4
	ds_read2_b32 v[168:169], v177 offset0:8 offset1:12
	s_waitcnt vmcnt(10)
	ds_read2_b32 v[184:185], v177 offset0:16 offset1:20
	s_waitcnt vmcnt(9)
	ds_read2_b32 v[190:191], v177 offset0:24 offset1:28
	v_cvt_scalef32_pk32_f32_fp6 v[96:127], v[134:139], 1.0
	v_cvt_scalef32_pk32_f32_fp6 v[64:95], v[128:133], 1.0
	ds_read_u16 v129, v152 offset:64
	ds_read_u16 v131, v152 offset:72
	ds_read_u16 v132, v152 offset:80
	ds_read_u16 v133, v152 offset:88
	ds_read_u16 v134, v152 offset:96
	ds_read_u16 v135, v152 offset:104
	ds_read_u16 v136, v152 offset:112
	ds_read_u16 v137, v152 offset:120
	s_waitcnt lgkmcnt(11)
	v_pk_fma_f32 v[96:97], v[96:97], v[166:167], 0 op_sel_hi:[1,0,0]
	v_pk_fma_f32 v[98:99], v[98:99], v[166:167], 0 op_sel_hi:[1,0,0]
	v_pk_fma_f32 v[100:101], v[100:101], v[166:167], 0 op_sel_hi:[1,0,0]
	v_pk_fma_f32 v[102:103], v[102:103], v[166:167], 0 op_sel_hi:[1,0,0]
	v_pk_fma_f32 v[104:105], v[104:105], v[166:167], 0 op_sel_hi:[1,0,0]
	v_pk_fma_f32 v[106:107], v[106:107], v[166:167], 0 op_sel_hi:[1,0,0]
	v_pk_fma_f32 v[108:109], v[108:109], v[166:167], 0 op_sel_hi:[1,0,0]
	v_pk_fma_f32 v[110:111], v[110:111], v[166:167], 0 op_sel_hi:[1,0,0]
	v_mov_b32_e32 v128, v167
	s_waitcnt lgkmcnt(7)
	v_pk_fma_f32 v[96:97], v[112:113], v[128:129], v[96:97] op_sel_hi:[1,0,1]
	v_pk_fma_f32 v[98:99], v[114:115], v[128:129], v[98:99] op_sel_hi:[1,0,1]
	v_pk_fma_f32 v[100:101], v[116:117], v[128:129], v[100:101] op_sel_hi:[1,0,1]
	v_pk_fma_f32 v[102:103], v[118:119], v[128:129], v[102:103] op_sel_hi:[1,0,1]
	v_pk_fma_f32 v[104:105], v[120:121], v[128:129], v[104:105] op_sel_hi:[1,0,1]
	v_pk_fma_f32 v[106:107], v[122:123], v[128:129], v[106:107] op_sel_hi:[1,0,1]
	v_pk_fma_f32 v[108:109], v[124:125], v[128:129], v[108:109] op_sel_hi:[1,0,1]
	v_pk_fma_f32 v[110:111], v[126:127], v[128:129], v[110:111] op_sel_hi:[1,0,1]
	v_add_u32_e32 v112, s21, v129
	v_mov_b32_e32 v130, v169
	s_waitcnt lgkmcnt(6)
	v_add_u32_e32 v113, s21, v131
	s_waitcnt lgkmcnt(5)
	v_add_u32_e32 v114, s21, v132
	s_waitcnt lgkmcnt(4)
	v_add_u32_e32 v115, s21, v133
	s_waitcnt lgkmcnt(3)
	v_add_u32_e32 v116, s21, v134
	s_waitcnt lgkmcnt(2)
	v_add_u32_e32 v117, s21, v135
	s_waitcnt lgkmcnt(1)
	v_add_u32_e32 v118, s21, v136
	s_waitcnt lgkmcnt(0)
	v_add_u32_e32 v119, s21, v137
	v_pk_fma_f32 v[64:65], v[64:65], v[168:169], v[96:97] op_sel_hi:[1,0,1]
	v_pk_fma_f32 v[66:67], v[66:67], v[168:169], v[98:99] op_sel_hi:[1,0,1]
	v_pk_fma_f32 v[68:69], v[68:69], v[168:169], v[100:101] op_sel_hi:[1,0,1]
	v_pk_fma_f32 v[70:71], v[70:71], v[168:169], v[102:103] op_sel_hi:[1,0,1]
	v_pk_fma_f32 v[72:73], v[72:73], v[168:169], v[104:105] op_sel_hi:[1,0,1]
	v_pk_fma_f32 v[74:75], v[74:75], v[168:169], v[106:107] op_sel_hi:[1,0,1]
	v_pk_fma_f32 v[76:77], v[76:77], v[168:169], v[108:109] op_sel_hi:[1,0,1]
	v_pk_fma_f32 v[78:79], v[78:79], v[168:169], v[110:111] op_sel_hi:[1,0,1]
	v_mad_u64_u32 v[96:97], s[30:31], v112, s16, v[160:161]
	v_cvt_scalef32_pk32_f32_fp6 v[32:63], v[140:145], 1.0
	v_mad_u64_u32 v[98:99], s[30:31], v113, s16, v[160:161]
	v_mad_u64_u32 v[100:101], s[30:31], v114, s16, v[160:161]
	v_mad_u64_u32 v[102:103], s[30:31], v115, s16, v[160:161]
	v_mad_u64_u32 v[104:105], s[30:31], v116, s16, v[160:161]
	v_mad_u64_u32 v[106:107], s[30:31], v117, s16, v[160:161]
	v_mad_u64_u32 v[108:109], s[30:31], v118, s16, v[160:161]
	v_mad_u64_u32 v[110:111], s[30:31], v119, s16, v[160:161]
	v_pk_fma_f32 v[64:65], v[80:81], v[130:131], v[64:65] op_sel_hi:[1,0,1]
	v_pk_fma_f32 v[66:67], v[82:83], v[130:131], v[66:67] op_sel_hi:[1,0,1]
	v_pk_fma_f32 v[68:69], v[84:85], v[130:131], v[68:69] op_sel_hi:[1,0,1]
	v_pk_fma_f32 v[70:71], v[86:87], v[130:131], v[70:71] op_sel_hi:[1,0,1]
	v_pk_fma_f32 v[72:73], v[88:89], v[130:131], v[72:73] op_sel_hi:[1,0,1]
	v_pk_fma_f32 v[74:75], v[90:91], v[130:131], v[74:75] op_sel_hi:[1,0,1]
	v_pk_fma_f32 v[76:77], v[92:93], v[130:131], v[76:77] op_sel_hi:[1,0,1]
; #define P12_VISSUE(c_, i_, q_, D_X) do { _Pragma("unroll") for (int b = 0; b < 8; ++b) { const int idx = ((q_) * 8 + b) * 4 + eg; const unsigned ro = (unsigned)(c_) * 16384u + (unsigned)EL[(i_) * 128 + idx]; \
;           const v3u_ ld_ = *(const v3u_*)(V8 + (size_t)(ro * 192u + 12u * (unsigned)cl)); if (b & 1) D_X[b >> 1].hi = ld_; else D_X[b >> 1].lo = ld_; } } while (0)
; __device__ __forceinline__ void p12_peer(Frame& F) {
;     ...
;               P12_VISSUE(c, i, 1, dB); asm volatile("" ::: "memory"); P12_VCOMP(i, 0, dA);
;               P12_VISSUE(c, i, 2, dA); asm volatile("" ::: "memory"); P12_VCOMP(i, 1, dB);
;               P12_VISSUE(c, i, 3, dB); asm volatile("" ::: "memory"); P12_VCOMP(i, 2, dA);
	v_pk_fma_f32 v[78:79], v[94:95], v[130:131], v[78:79] op_sel_hi:[1,0,1]
	global_load_dwordx3 v[198:200], v96, s[2:3]
	global_load_dwordx3 v[128:130], v98, s[2:3]
	global_load_dwordx3 v[204:206], v100, s[2:3]
	global_load_dwordx3 v[132:134], v102, s[2:3]
	global_load_dwordx3 v[210:212], v104, s[2:3]
	global_load_dwordx3 v[136:138], v106, s[2:3]
	global_load_dwordx3 v[216:218], v108, s[2:3]
	global_load_dwordx3 v[140:142], v110, s[2:3]
	v_mov_b32_e32 v144, v185
	v_pk_fma_f32 v[32:33], v[32:33], v[184:185], v[64:65] op_sel_hi:[1,0,1]
	v_pk_fma_f32 v[34:35], v[34:35], v[184:185], v[66:67] op_sel_hi:[1,0,1]
	v_pk_fma_f32 v[36:37], v[36:37], v[184:185], v[68:69] op_sel_hi:[1,0,1]
	v_pk_fma_f32 v[38:39], v[38:39], v[184:185], v[70:71] op_sel_hi:[1,0,1]
	v_pk_fma_f32 v[40:41], v[40:41], v[184:185], v[72:73] op_sel_hi:[1,0,1]
	v_pk_fma_f32 v[42:43], v[42:43], v[184:185], v[74:75] op_sel_hi:[1,0,1]
	v_pk_fma_f32 v[44:45], v[44:45], v[184:185], v[76:77] op_sel_hi:[1,0,1]
	v_pk_fma_f32 v[46:47], v[46:47], v[184:185], v[78:79] op_sel_hi:[1,0,1]
	v_cvt_scalef32_pk32_f32_fp6 v[0:31], v[146:151], 1.0
	v_pk_fma_f32 v[32:33], v[48:49], v[144:145], v[32:33] op_sel_hi:[1,0,1]
	v_pk_fma_f32 v[34:35], v[50:51], v[144:145], v[34:35] op_sel_hi:[1,0,1]
	v_pk_fma_f32 v[36:37], v[52:53], v[144:145], v[36:37] op_sel_hi:[1,0,1]
	v_pk_fma_f32 v[38:39], v[54:55], v[144:145], v[38:39] op_sel_hi:[1,0,1]
	v_pk_fma_f32 v[40:41], v[56:57], v[144:145], v[40:41] op_sel_hi:[1,0,1]
	v_pk_fma_f32 v[42:43], v[58:59], v[144:145], v[42:43] op_sel_hi:[1,0,1]
	v_pk_fma_f32 v[44:45], v[60:61], v[144:145], v[44:45] op_sel_hi:[1,0,1]
	v_pk_fma_f32 v[46:47], v[62:63], v[144:145], v[46:47] op_sel_hi:[1,0,1]
	s_waitcnt vmcnt(16)
	v_lshlrev_b32_e32 v167, 16, v159
	v_lshlrev_b32_e32 v166, 16, v158
	v_and_b32_e32 v169, 0xffff0000, v159
	v_and_b32_e32 v168, 0xffff0000, v158
	s_waitcnt vmcnt(14)
	v_mov_b32_e32 v157, v220
	v_mov_b32_e32 v158, v221
	v_mov_b32_e32 v159, v222
	v_mov_b32_e32 v146, v191
	v_pk_fma_f32 v[0:1], v[0:1], v[190:191], v[32:33] op_sel_hi:[1,0,1]
	v_pk_fma_f32 v[2:3], v[2:3], v[190:191], v[34:35] op_sel_hi:[1,0,1]
	v_pk_fma_f32 v[4:5], v[4:5], v[190:191], v[36:37] op_sel_hi:[1,0,1]
	v_pk_fma_f32 v[6:7], v[6:7], v[190:191], v[38:39] op_sel_hi:[1,0,1]
	v_pk_fma_f32 v[8:9], v[8:9], v[190:191], v[40:41] op_sel_hi:[1,0,1]
	v_pk_fma_f32 v[10:11], v[10:11], v[190:191], v[42:43] op_sel_hi:[1,0,1]
	v_pk_fma_f32 v[12:13], v[12:13], v[190:191], v[44:45] op_sel_hi:[1,0,1]
	v_pk_fma_f32 v[14:15], v[14:15], v[190:191], v[46:47] op_sel_hi:[1,0,1]
	s_waitcnt vmcnt(12)
	v_mov_b32_e32 v183, v224
	v_mov_b32_e32 v184, v225
	v_mov_b32_e32 v185, v226
	s_waitcnt vmcnt(10)
	v_mov_b32_e32 v189, v228
	v_mov_b32_e32 v190, v229
	v_mov_b32_e32 v191, v230
	s_waitcnt vmcnt(8)
	v_mov_b32_e32 v195, v232
	v_mov_b32_e32 v196, v233
	v_mov_b32_e32 v197, v234
	ds_read2_b32 v[220:221], v177 offset0:32 offset1:36
	ds_read2_b32 v[222:223], v177 offset0:40 offset1:44
	ds_read2_b32 v[242:243], v177 offset0:48 offset1:52
	ds_read2_b32 v[244:245], v177 offset0:56 offset1:60
	v_cvt_scalef32_pk32_f32_fp6 v[96:127], v[154:159], 1.0
	ds_read_u16 v131, v152 offset:128
	ds_read_u16 v135, v152 offset:136
	ds_read_u16 v139, v152 offset:144
	ds_read_u16 v143, v152 offset:152
	ds_read_u16 v153, v152 offset:160
	ds_read_u16 v154, v152 offset:168
	ds_read_u16 v155, v152 offset:176
	ds_read_u16 v152, v152 offset:184
	v_pk_fma_f32 v[144:145], v[16:17], v[146:147], v[0:1] op_sel_hi:[1,0,1]
	v_pk_fma_f32 v[148:149], v[18:19], v[146:147], v[2:3] op_sel_hi:[1,0,1]
	v_pk_fma_f32 v[150:151], v[20:21], v[146:147], v[4:5] op_sel_hi:[1,0,1]
	v_pk_fma_f32 v[202:203], v[22:23], v[146:147], v[6:7] op_sel_hi:[1,0,1]
	v_pk_fma_f32 v[208:209], v[24:25], v[146:147], v[8:9] op_sel_hi:[1,0,1]
	v_pk_fma_f32 v[214:215], v[26:27], v[146:147], v[10:11] op_sel_hi:[1,0,1]
	v_pk_fma_f32 v[236:237], v[28:29], v[146:147], v[12:13] op_sel_hi:[1,0,1]
	v_pk_fma_f32 v[146:147], v[30:31], v[146:147], v[14:15] op_sel_hi:[1,0,1]
	s_waitcnt lgkmcnt(11)
	v_pk_fma_f32 v[96:97], v[96:97], v[220:221], v[144:145] op_sel_hi:[1,0,1]
	v_mov_b32_e32 v144, v221
	v_cvt_scalef32_pk32_f32_fp6 v[64:95], v[180:185], 1.0
	v_pk_fma_f32 v[98:99], v[98:99], v[220:221], v[148:149] op_sel_hi:[1,0,1]
	v_pk_fma_f32 v[100:101], v[100:101], v[220:221], v[150:151] op_sel_hi:[1,0,1]
	v_pk_fma_f32 v[102:103], v[102:103], v[220:221], v[202:203] op_sel_hi:[1,0,1]
	v_pk_fma_f32 v[104:105], v[104:105], v[220:221], v[208:209] op_sel_hi:[1,0,1]
	v_pk_fma_f32 v[106:107], v[106:107], v[220:221], v[214:215] op_sel_hi:[1,0,1]
	v_pk_fma_f32 v[108:109], v[108:109], v[220:221], v[236:237] op_sel_hi:[1,0,1]
	v_pk_fma_f32 v[110:111], v[110:111], v[220:221], v[146:147] op_sel_hi:[1,0,1]
	v_pk_fma_f32 v[96:97], v[112:113], v[144:145], v[96:97] op_sel_hi:[1,0,1]
	s_waitcnt lgkmcnt(7)
	v_add_u32_e32 v112, s21, v131
	v_pk_fma_f32 v[98:99], v[114:115], v[144:145], v[98:99] op_sel_hi:[1,0,1]
	v_pk_fma_f32 v[100:101], v[116:117], v[144:145], v[100:101] op_sel_hi:[1,0,1]
	v_pk_fma_f32 v[102:103], v[118:119], v[144:145], v[102:103] op_sel_hi:[1,0,1]
	v_pk_fma_f32 v[104:105], v[120:121], v[144:145], v[104:105] op_sel_hi:[1,0,1]
	v_pk_fma_f32 v[106:107], v[122:123], v[144:145], v[106:107] op_sel_hi:[1,0,1]
	v_pk_fma_f32 v[108:109], v[124:125], v[144:145], v[108:109] op_sel_hi:[1,0,1]
	v_pk_fma_f32 v[110:111], v[126:127], v[144:145], v[110:111] op_sel_hi:[1,0,1]
	s_waitcnt lgkmcnt(6)
	v_add_u32_e32 v113, s21, v135
	s_waitcnt lgkmcnt(5)
	v_add_u32_e32 v114, s21, v139
	s_waitcnt lgkmcnt(4)
	v_add_u32_e32 v115, s21, v143
	s_waitcnt lgkmcnt(3)
	v_add_u32_e32 v116, s21, v153
	s_waitcnt lgkmcnt(2)
; #define P12_VISSUE(c_, i_, q_, D_X) do { _Pragma("unroll") for (int b = 0; b < 8; ++b) { const int idx = ((q_) * 8 + b) * 4 + eg; const unsigned ro = (unsigned)(c_) * 16384u + (unsigned)EL[(i_) * 128 + idx]; \
;           const v3u_ ld_ = *(const v3u_*)(V8 + (size_t)(ro * 192u + 12u * (unsigned)cl)); if (b & 1) D_X[b >> 1].hi = ld_; else D_X[b >> 1].lo = ld_; } } while (0)
; __device__ __forceinline__ void p12_peer(Frame& F) {
;     ...
;               P12_VISSUE(c, i, 1, dB); asm volatile("" ::: "memory"); P12_VCOMP(i, 0, dA);
;               P12_VISSUE(c, i, 2, dA); asm volatile("" ::: "memory"); P12_VCOMP(i, 1, dB);
;               P12_VISSUE(c, i, 3, dB); asm volatile("" ::: "memory"); P12_VCOMP(i, 2, dA);
	v_add_u32_e32 v117, s21, v154
	s_waitcnt lgkmcnt(1)
	v_add_u32_e32 v118, s21, v155
	s_waitcnt lgkmcnt(0)
	v_add_u32_e32 v119, s21, v152
	v_pk_fma_f32 v[64:65], v[64:65], v[222:223], v[96:97] op_sel_hi:[1,0,1]
	v_mad_u64_u32 v[96:97], s[30:31], v112, s16, v[160:161]
	v_cvt_scalef32_pk32_f32_fp6 v[32:63], v[186:191], 1.0
	v_cvt_scalef32_pk32_f32_fp6 v[0:31], v[192:197], 1.0
	v_mov_b32_e32 v146, v223
	v_pk_fma_f32 v[66:67], v[66:67], v[222:223], v[98:99] op_sel_hi:[1,0,1]
	v_pk_fma_f32 v[68:69], v[68:69], v[222:223], v[100:101] op_sel_hi:[1,0,1]
	v_pk_fma_f32 v[70:71], v[70:71], v[222:223], v[102:103] op_sel_hi:[1,0,1]
	v_pk_fma_f32 v[72:73], v[72:73], v[222:223], v[104:105] op_sel_hi:[1,0,1]
	v_pk_fma_f32 v[74:75], v[74:75], v[222:223], v[106:107] op_sel_hi:[1,0,1]
	v_pk_fma_f32 v[76:77], v[76:77], v[222:223], v[108:109] op_sel_hi:[1,0,1]
	v_pk_fma_f32 v[78:79], v[78:79], v[222:223], v[110:111] op_sel_hi:[1,0,1]
	v_mad_u64_u32 v[98:99], s[30:31], v113, s16, v[160:161]
	v_mad_u64_u32 v[100:101], s[30:31], v114, s16, v[160:161]
	v_mad_u64_u32 v[102:103], s[30:31], v115, s16, v[160:161]
	v_mad_u64_u32 v[104:105], s[30:31], v116, s16, v[160:161]
	v_mad_u64_u32 v[106:107], s[30:31], v117, s16, v[160:161]
	v_mad_u64_u32 v[108:109], s[30:31], v118, s16, v[160:161]
	v_mad_u64_u32 v[110:111], s[30:31], v119, s16, v[160:161]
	global_load_dwordx3 v[180:182], v96, s[2:3]
	global_load_dwordx3 v[226:228], v98, s[2:3]
	global_load_dwordx3 v[186:188], v100, s[2:3]
	global_load_dwordx3 v[230:232], v102, s[2:3]
	global_load_dwordx3 v[192:194], v104, s[2:3]
	global_load_dwordx3 v[234:236], v106, s[2:3]
	global_load_dwordx3 v[222:224], v108, s[2:3]
	global_load_dwordx3 v[238:240], v110, s[2:3]
	s_waitcnt vmcnt(14)
	v_mov_b32_e32 v201, v128
	v_mov_b32_e32 v202, v129
	v_mov_b32_e32 v203, v130
	s_waitcnt vmcnt(12)
	v_mov_b32_e32 v207, v132
	v_mov_b32_e32 v208, v133
	v_mov_b32_e32 v209, v134
	s_waitcnt vmcnt(10)
	v_mov_b32_e32 v213, v136
	v_mov_b32_e32 v214, v137
	v_mov_b32_e32 v215, v138
	s_waitcnt vmcnt(8)
	v_mov_b32_e32 v219, v140
	v_mov_b32_e32 v220, v141
	v_mov_b32_e32 v221, v142
	v_pk_fma_f32 v[64:65], v[80:81], v[146:147], v[64:65] op_sel_hi:[1,0,1]
	v_pk_fma_f32 v[66:67], v[82:83], v[146:147], v[66:67] op_sel_hi:[1,0,1]
	v_pk_fma_f32 v[68:69], v[84:85], v[146:147], v[68:69] op_sel_hi:[1,0,1]
	v_pk_fma_f32 v[70:71], v[86:87], v[146:147], v[70:71] op_sel_hi:[1,0,1]
	v_pk_fma_f32 v[72:73], v[88:89], v[146:147], v[72:73] op_sel_hi:[1,0,1]
	v_pk_fma_f32 v[74:75], v[90:91], v[146:147], v[74:75] op_sel_hi:[1,0,1]
	v_pk_fma_f32 v[76:77], v[92:93], v[146:147], v[76:77] op_sel_hi:[1,0,1]
	v_pk_fma_f32 v[78:79], v[94:95], v[146:147], v[78:79] op_sel_hi:[1,0,1]
	ds_read2_b32 v[196:197], v177 offset0:64 offset1:68
	v_mov_b32_e32 v184, v243
	ds_read2_b32 v[246:247], v177 offset0:72 offset1:76
	ds_read2_b32 v[248:249], v177 offset0:80 offset1:84
	ds_read2_b32 v[250:251], v177 offset0:88 offset1:92
	v_pk_fma_f32 v[32:33], v[32:33], v[242:243], v[64:65] op_sel_hi:[1,0,1]
	v_pk_fma_f32 v[34:35], v[34:35], v[242:243], v[66:67] op_sel_hi:[1,0,1]
	v_pk_fma_f32 v[36:37], v[36:37], v[242:243], v[68:69] op_sel_hi:[1,0,1]
	v_pk_fma_f32 v[38:39], v[38:39], v[242:243], v[70:71] op_sel_hi:[1,0,1]
	v_pk_fma_f32 v[40:41], v[40:41], v[242:243], v[72:73] op_sel_hi:[1,0,1]
	v_pk_fma_f32 v[42:43], v[42:43], v[242:243], v[74:75] op_sel_hi:[1,0,1]
	v_pk_fma_f32 v[44:45], v[44:45], v[242:243], v[76:77] op_sel_hi:[1,0,1]
	v_pk_fma_f32 v[46:47], v[46:47], v[242:243], v[78:79] op_sel_hi:[1,0,1]
	v_cvt_scalef32_pk32_f32_fp6 v[128:159], v[198:203], 1.0
	v_cvt_scalef32_pk32_f32_fp6 v[96:127], v[204:209], 1.0
	v_cvt_scalef32_pk32_f32_fp6 v[64:95], v[210:215], 1.0
	v_pk_fma_f32 v[198:199], v[48:49], v[184:185], v[32:33] op_sel_hi:[1,0,1]
	v_pk_fma_f32 v[200:201], v[50:51], v[184:185], v[34:35] op_sel_hi:[1,0,1]
	v_pk_fma_f32 v[202:203], v[52:53], v[184:185], v[36:37] op_sel_hi:[1,0,1]
	v_pk_fma_f32 v[204:205], v[54:55], v[184:185], v[38:39] op_sel_hi:[1,0,1]
	v_pk_fma_f32 v[206:207], v[56:57], v[184:185], v[40:41] op_sel_hi:[1,0,1]
	v_pk_fma_f32 v[208:209], v[58:59], v[184:185], v[42:43] op_sel_hi:[1,0,1]
	v_pk_fma_f32 v[210:211], v[60:61], v[184:185], v[44:45] op_sel_hi:[1,0,1]
	v_pk_fma_f32 v[184:185], v[62:63], v[184:185], v[46:47] op_sel_hi:[1,0,1]
	ds_read_u16 v183, v179 offset:16384
	ds_read_u16 v189, v179 offset:16392
	ds_read_u16 v191, v179 offset:16400
	ds_read_u16 v195, v179 offset:16408
	ds_read_u16 v212, v179 offset:16416
	ds_read_u16 v213, v179 offset:16424
	ds_read_u16 v214, v179 offset:16432
	ds_read_u16 v179, v179 offset:16440
	v_mov_b32_e32 v190, v245
	v_pk_fma_f32 v[0:1], v[0:1], v[244:245], v[198:199] op_sel_hi:[1,0,1]
	v_pk_fma_f32 v[2:3], v[2:3], v[244:245], v[200:201] op_sel_hi:[1,0,1]
	v_pk_fma_f32 v[4:5], v[4:5], v[244:245], v[202:203] op_sel_hi:[1,0,1]
	v_pk_fma_f32 v[6:7], v[6:7], v[244:245], v[204:205] op_sel_hi:[1,0,1]
	v_pk_fma_f32 v[8:9], v[8:9], v[244:245], v[206:207] op_sel_hi:[1,0,1]
	v_pk_fma_f32 v[10:11], v[10:11], v[244:245], v[208:209] op_sel_hi:[1,0,1]
	v_pk_fma_f32 v[12:13], v[12:13], v[244:245], v[210:211] op_sel_hi:[1,0,1]
	v_pk_fma_f32 v[14:15], v[14:15], v[244:245], v[184:185] op_sel_hi:[1,0,1]
	s_cselect_b32 s29, s22, s17
	s_waitcnt lgkmcnt(5)
; #define P12_VISSUE(c_, i_, q_, D_X) do { _Pragma("unroll") for (int b = 0; b < 8; ++b) { const int idx = ((q_) * 8 + b) * 4 + eg; const unsigned ro = (unsigned)(c_) * 16384u + (unsigned)EL[(i_) * 128 + idx]; \
;           const v3u_ ld_ = *(const v3u_*)(V8 + (size_t)(ro * 192u + 12u * (unsigned)cl)); if (b & 1) D_X[b >> 1].hi = ld_; else D_X[b >> 1].lo = ld_; } } while (0)
; __device__ __forceinline__ void p12_peer(Frame& F) {
;     ...
;               P12_VISSUE(c, i, 1, dB); asm volatile("" ::: "memory"); P12_VCOMP(i, 0, dA);
;               P12_VISSUE(c, i, 2, dA); asm volatile("" ::: "memory"); P12_VCOMP(i, 1, dB);
;               P12_VISSUE(c, i, 3, dB); asm volatile("" ::: "memory"); P12_VCOMP(i, 2, dA);
;               { const int in_ = i + 1 < 4 ? i + 1 : 0, cn_ = i + 1 < 4 ? c : (c + 1 < 16 ? c + 1 : 15); P12_VISSUE(cn_, in_, 0, dA); } asm volatile("" ::: "memory"); P12_VCOMP(i, 3, dB);
	v_pk_fma_f32 v[0:1], v[16:17], v[190:191], v[0:1] op_sel_hi:[1,0,1]
	v_pk_fma_f32 v[2:3], v[18:19], v[190:191], v[2:3] op_sel_hi:[1,0,1]
	v_pk_fma_f32 v[4:5], v[20:21], v[190:191], v[4:5] op_sel_hi:[1,0,1]
	v_pk_fma_f32 v[6:7], v[22:23], v[190:191], v[6:7] op_sel_hi:[1,0,1]
	v_pk_fma_f32 v[8:9], v[24:25], v[190:191], v[8:9] op_sel_hi:[1,0,1]
	v_pk_fma_f32 v[10:11], v[26:27], v[190:191], v[10:11] op_sel_hi:[1,0,1]
	v_pk_fma_f32 v[12:13], v[28:29], v[190:191], v[12:13] op_sel_hi:[1,0,1]
	v_pk_fma_f32 v[14:15], v[30:31], v[190:191], v[14:15] op_sel_hi:[1,0,1]
	s_lshl_b64 s[14:15], s[12:13], 14
	s_lshl_b32 s13, s29, 14
	v_pk_fma_f32 v[0:1], v[128:129], v[196:197], v[0:1] op_sel_hi:[1,0,1]
	v_pk_fma_f32 v[2:3], v[130:131], v[196:197], v[2:3] op_sel_hi:[1,0,1]
	v_pk_fma_f32 v[4:5], v[132:133], v[196:197], v[4:5] op_sel_hi:[1,0,1]
	v_pk_fma_f32 v[6:7], v[134:135], v[196:197], v[6:7] op_sel_hi:[1,0,1]
	v_pk_fma_f32 v[8:9], v[136:137], v[196:197], v[8:9] op_sel_hi:[1,0,1]
	v_pk_fma_f32 v[10:11], v[138:139], v[196:197], v[10:11] op_sel_hi:[1,0,1]
	v_pk_fma_f32 v[12:13], v[140:141], v[196:197], v[12:13] op_sel_hi:[1,0,1]
	v_pk_fma_f32 v[14:15], v[142:143], v[196:197], v[14:15] op_sel_hi:[1,0,1]
	v_mov_b32_e32 v16, v197
	v_pk_fma_f32 v[0:1], v[144:145], v[16:17], v[0:1] op_sel_hi:[1,0,1]
	v_pk_fma_f32 v[2:3], v[146:147], v[16:17], v[2:3] op_sel_hi:[1,0,1]
	v_pk_fma_f32 v[4:5], v[148:149], v[16:17], v[4:5] op_sel_hi:[1,0,1]
	v_pk_fma_f32 v[6:7], v[150:151], v[16:17], v[6:7] op_sel_hi:[1,0,1]
	v_pk_fma_f32 v[8:9], v[152:153], v[16:17], v[8:9] op_sel_hi:[1,0,1]
	v_pk_fma_f32 v[10:11], v[154:155], v[16:17], v[10:11] op_sel_hi:[1,0,1]
	v_pk_fma_f32 v[12:13], v[156:157], v[16:17], v[12:13] op_sel_hi:[1,0,1]
	v_pk_fma_f32 v[14:15], v[158:159], v[16:17], v[14:15] op_sel_hi:[1,0,1]
	v_add_u32_e32 v16, s13, v183
	v_add_u32_e32 v19, s13, v189
	v_add_u32_e32 v21, s13, v191
	s_waitcnt lgkmcnt(4)
	v_add_u32_e32 v23, s13, v195
	s_waitcnt lgkmcnt(3)
	v_add_u32_e32 v30, s13, v212
	s_waitcnt lgkmcnt(2)
	v_add_u32_e32 v128, s13, v213
	s_waitcnt lgkmcnt(1)
	v_add_u32_e32 v129, s13, v214
	s_waitcnt lgkmcnt(0)
	v_add_u32_e32 v130, s13, v179
	v_mad_u64_u32 v[16:17], s[30:31], v16, s16, v[160:161]
	v_pk_fma_f32 v[0:1], v[96:97], v[246:247], v[0:1] op_sel_hi:[1,0,1]
	v_pk_fma_f32 v[2:3], v[98:99], v[246:247], v[2:3] op_sel_hi:[1,0,1]
	v_pk_fma_f32 v[4:5], v[100:101], v[246:247], v[4:5] op_sel_hi:[1,0,1]
	v_mad_u64_u32 v[24:25], s[30:31], v19, s16, v[160:161]
	v_mad_u64_u32 v[26:27], s[30:31], v21, s16, v[160:161]
	v_mad_u64_u32 v[28:29], s[30:31], v23, s16, v[160:161]
	v_mad_u64_u32 v[30:31], s[30:31], v30, s16, v[160:161]
	v_mad_u64_u32 v[96:97], s[30:31], v128, s16, v[160:161]
	v_mad_u64_u32 v[98:99], s[30:31], v129, s16, v[160:161]
	v_mad_u64_u32 v[100:101], s[30:31], v130, s16, v[160:161]
	global_load_dwordx3 v[134:136], v16, s[2:3]
	global_load_dwordx3 v[152:154], v24, s[2:3]
	global_load_dwordx3 v[128:130], v26, s[2:3]
	global_load_dwordx3 v[156:158], v28, s[2:3]
	global_load_dwordx3 v[140:142], v30, s[2:3]
	global_load_dwordx3 v[198:200], v96, s[2:3]
	global_load_dwordx3 v[146:148], v98, s[2:3]
	global_load_dwordx3 v[202:204], v100, s[2:3]
	v_mov_b32_e32 v18, v247
	v_pk_fma_f32 v[6:7], v[102:103], v[246:247], v[6:7] op_sel_hi:[1,0,1]
	v_pk_fma_f32 v[8:9], v[104:105], v[246:247], v[8:9] op_sel_hi:[1,0,1]
	v_pk_fma_f32 v[10:11], v[106:107], v[246:247], v[10:11] op_sel_hi:[1,0,1]
	v_pk_fma_f32 v[12:13], v[108:109], v[246:247], v[12:13] op_sel_hi:[1,0,1]
	v_pk_fma_f32 v[14:15], v[110:111], v[246:247], v[14:15] op_sel_hi:[1,0,1]
	s_waitcnt vmcnt(14)
	v_mov_b32_e32 v183, v226
	v_mov_b32_e32 v184, v227
	v_mov_b32_e32 v185, v228
	v_pk_fma_f32 v[0:1], v[112:113], v[18:19], v[0:1] op_sel_hi:[1,0,1]
	v_pk_fma_f32 v[2:3], v[114:115], v[18:19], v[2:3] op_sel_hi:[1,0,1]
	v_pk_fma_f32 v[4:5], v[116:117], v[18:19], v[4:5] op_sel_hi:[1,0,1]
	v_pk_fma_f32 v[6:7], v[118:119], v[18:19], v[6:7] op_sel_hi:[1,0,1]
	v_pk_fma_f32 v[8:9], v[120:121], v[18:19], v[8:9] op_sel_hi:[1,0,1]
	v_pk_fma_f32 v[10:11], v[122:123], v[18:19], v[10:11] op_sel_hi:[1,0,1]
	v_pk_fma_f32 v[12:13], v[124:125], v[18:19], v[12:13] op_sel_hi:[1,0,1]
	v_pk_fma_f32 v[14:15], v[126:127], v[18:19], v[14:15] op_sel_hi:[1,0,1]
	ds_read2_b32 v[214:215], v177 offset0:96 offset1:100
	v_mov_b32_e32 v20, v249
	v_pk_fma_f32 v[0:1], v[64:65], v[248:249], v[0:1] op_sel_hi:[1,0,1]
	v_pk_fma_f32 v[2:3], v[66:67], v[248:249], v[2:3] op_sel_hi:[1,0,1]
	v_pk_fma_f32 v[4:5], v[68:69], v[248:249], v[4:5] op_sel_hi:[1,0,1]
	v_pk_fma_f32 v[6:7], v[70:71], v[248:249], v[6:7] op_sel_hi:[1,0,1]
	v_pk_fma_f32 v[8:9], v[72:73], v[248:249], v[8:9] op_sel_hi:[1,0,1]
	v_pk_fma_f32 v[10:11], v[74:75], v[248:249], v[10:11] op_sel_hi:[1,0,1]
	v_pk_fma_f32 v[12:13], v[76:77], v[248:249], v[12:13] op_sel_hi:[1,0,1]
	v_pk_fma_f32 v[14:15], v[78:79], v[248:249], v[14:15] op_sel_hi:[1,0,1]
	s_waitcnt vmcnt(12)
	v_mov_b32_e32 v189, v230
	v_mov_b32_e32 v190, v231
	v_mov_b32_e32 v191, v232
	v_cvt_scalef32_pk32_f32_fp6 v[32:63], v[216:221], 1.0
	v_pk_fma_f32 v[0:1], v[80:81], v[20:21], v[0:1] op_sel_hi:[1,0,1]
	v_pk_fma_f32 v[2:3], v[82:83], v[20:21], v[2:3] op_sel_hi:[1,0,1]
	v_pk_fma_f32 v[4:5], v[84:85], v[20:21], v[4:5] op_sel_hi:[1,0,1]
	v_pk_fma_f32 v[6:7], v[86:87], v[20:21], v[6:7] op_sel_hi:[1,0,1]
	v_pk_fma_f32 v[8:9], v[88:89], v[20:21], v[8:9] op_sel_hi:[1,0,1]
	v_pk_fma_f32 v[10:11], v[90:91], v[20:21], v[10:11] op_sel_hi:[1,0,1]
	v_pk_fma_f32 v[12:13], v[92:93], v[20:21], v[12:13] op_sel_hi:[1,0,1]
	v_pk_fma_f32 v[14:15], v[94:95], v[20:21], v[14:15] op_sel_hi:[1,0,1]
	ds_read2_b32 v[216:217], v177 offset0:104 offset1:108
	v_mov_b32_e32 v22, v251
	v_pk_fma_f32 v[0:1], v[32:33], v[250:251], v[0:1] op_sel_hi:[1,0,1]
	v_pk_fma_f32 v[2:3], v[34:35], v[250:251], v[2:3] op_sel_hi:[1,0,1]
	v_pk_fma_f32 v[4:5], v[36:37], v[250:251], v[4:5] op_sel_hi:[1,0,1]
	v_pk_fma_f32 v[6:7], v[38:39], v[250:251], v[6:7] op_sel_hi:[1,0,1]
	v_pk_fma_f32 v[8:9], v[40:41], v[250:251], v[8:9] op_sel_hi:[1,0,1]
	v_pk_fma_f32 v[10:11], v[42:43], v[250:251], v[10:11] op_sel_hi:[1,0,1]
	v_pk_fma_f32 v[12:13], v[44:45], v[250:251], v[12:13] op_sel_hi:[1,0,1]
	v_pk_fma_f32 v[14:15], v[46:47], v[250:251], v[14:15] op_sel_hi:[1,0,1]
	s_waitcnt vmcnt(10)
; #define P12_VISSUE(c_, i_, q_, D_X) do { _Pragma("unroll") for (int b = 0; b < 8; ++b) { const int idx = ((q_) * 8 + b) * 4 + eg; const unsigned ro = (unsigned)(c_) * 16384u + (unsigned)EL[(i_) * 128 + idx]; \
;           const v3u_ ld_ = *(const v3u_*)(V8 + (size_t)(ro * 192u + 12u * (unsigned)cl)); if (b & 1) D_X[b >> 1].hi = ld_; else D_X[b >> 1].lo = ld_; } } while (0)
; __device__ __forceinline__ void p12_peer(Frame& F) {
;     ...
;               { const int in_ = i + 1 < 4 ? i + 1 : 0, cn_ = i + 1 < 4 ? c : (c + 1 < 16 ? c + 1 : 15); P12_VISSUE(cn_, in_, 0, dA); } asm volatile("" ::: "memory"); P12_VCOMP(i, 3, dB);
	v_mov_b32_e32 v195, v234
	v_mov_b32_e32 v196, v235
	v_mov_b32_e32 v197, v236
	v_mov_b32_e32 v162, v176
	v_pk_fma_f32 v[132:133], v[48:49], v[22:23], v[0:1] op_sel_hi:[1,0,1]
	v_pk_fma_f32 v[138:139], v[50:51], v[22:23], v[2:3] op_sel_hi:[1,0,1]
	v_pk_fma_f32 v[144:145], v[52:53], v[22:23], v[4:5] op_sel_hi:[1,0,1]
	v_pk_fma_f32 v[150:151], v[54:55], v[22:23], v[6:7] op_sel_hi:[1,0,1]
	v_pk_fma_f32 v[206:207], v[56:57], v[22:23], v[8:9] op_sel_hi:[1,0,1]
	v_pk_fma_f32 v[208:209], v[58:59], v[22:23], v[10:11] op_sel_hi:[1,0,1]
	v_pk_fma_f32 v[210:211], v[60:61], v[22:23], v[12:13] op_sel_hi:[1,0,1]
	v_pk_fma_f32 v[212:213], v[62:63], v[22:23], v[14:15] op_sel_hi:[1,0,1]
	s_waitcnt vmcnt(8)
	v_mov_b32_e32 v225, v238
	v_mov_b32_e32 v226, v239
	v_mov_b32_e32 v227, v240
	ds_read2_b32 v[218:219], v177 offset0:112 offset1:116
	v_cvt_scalef32_pk32_f32_fp6 v[96:127], v[180:185], 1.0
	s_add_u32 s14, s26, s14
	ds_read2_b32 v[220:221], v177 offset0:120 offset1:124
	s_waitcnt lgkmcnt(3)
	v_pk_fma_f32 v[96:97], v[96:97], v[214:215], v[132:133] op_sel_hi:[1,0,1]
	v_pk_fma_f32 v[98:99], v[98:99], v[214:215], v[138:139] op_sel_hi:[1,0,1]
	v_pk_fma_f32 v[100:101], v[100:101], v[214:215], v[144:145] op_sel_hi:[1,0,1]
	v_pk_fma_f32 v[102:103], v[102:103], v[214:215], v[150:151] op_sel_hi:[1,0,1]
	v_pk_fma_f32 v[104:105], v[104:105], v[214:215], v[206:207] op_sel_hi:[1,0,1]
	v_pk_fma_f32 v[106:107], v[106:107], v[214:215], v[208:209] op_sel_hi:[1,0,1]
	v_pk_fma_f32 v[108:109], v[108:109], v[214:215], v[210:211] op_sel_hi:[1,0,1]
	v_pk_fma_f32 v[110:111], v[110:111], v[214:215], v[212:213] op_sel_hi:[1,0,1]
	v_mov_b32_e32 v132, v215
	s_addc_u32 s15, s27, s15
	v_cvt_scalef32_pk32_f32_fp6 v[64:95], v[186:191], 1.0
	v_add_u32_e32 v162, s18, v162
	v_pk_fma_f32 v[96:97], v[112:113], v[132:133], v[96:97] op_sel_hi:[1,0,1]
	v_pk_fma_f32 v[98:99], v[114:115], v[132:133], v[98:99] op_sel_hi:[1,0,1]
	v_pk_fma_f32 v[100:101], v[116:117], v[132:133], v[100:101] op_sel_hi:[1,0,1]
	v_pk_fma_f32 v[102:103], v[118:119], v[132:133], v[102:103] op_sel_hi:[1,0,1]
	v_pk_fma_f32 v[104:105], v[120:121], v[132:133], v[104:105] op_sel_hi:[1,0,1]
	v_pk_fma_f32 v[106:107], v[122:123], v[132:133], v[106:107] op_sel_hi:[1,0,1]
	v_pk_fma_f32 v[108:109], v[124:125], v[132:133], v[108:109] op_sel_hi:[1,0,1]
	v_pk_fma_f32 v[110:111], v[126:127], v[132:133], v[110:111] op_sel_hi:[1,0,1]
	v_lshl_add_u64 v[180:181], v[162:163], 2, s[14:15]
	s_waitcnt lgkmcnt(2)
	v_mov_b32_e32 v162, v217
	v_pk_fma_f32 v[64:65], v[64:65], v[216:217], v[96:97] op_sel_hi:[1,0,1]
	v_pk_fma_f32 v[66:67], v[66:67], v[216:217], v[98:99] op_sel_hi:[1,0,1]
	v_pk_fma_f32 v[68:69], v[68:69], v[216:217], v[100:101] op_sel_hi:[1,0,1]
	v_pk_fma_f32 v[70:71], v[70:71], v[216:217], v[102:103] op_sel_hi:[1,0,1]
	v_pk_fma_f32 v[72:73], v[72:73], v[216:217], v[104:105] op_sel_hi:[1,0,1]
	v_pk_fma_f32 v[74:75], v[74:75], v[216:217], v[106:107] op_sel_hi:[1,0,1]
	v_pk_fma_f32 v[76:77], v[76:77], v[216:217], v[108:109] op_sel_hi:[1,0,1]
	v_pk_fma_f32 v[78:79], v[78:79], v[216:217], v[110:111] op_sel_hi:[1,0,1]
	v_cvt_scalef32_pk32_f32_fp6 v[32:63], v[192:197], 1.0
	v_pk_fma_f32 v[64:65], v[80:81], v[162:163], v[64:65] op_sel_hi:[1,0,1]
	v_pk_fma_f32 v[66:67], v[82:83], v[162:163], v[66:67] op_sel_hi:[1,0,1]
	v_pk_fma_f32 v[68:69], v[84:85], v[162:163], v[68:69] op_sel_hi:[1,0,1]
	v_pk_fma_f32 v[70:71], v[86:87], v[162:163], v[70:71] op_sel_hi:[1,0,1]
	v_pk_fma_f32 v[72:73], v[88:89], v[162:163], v[72:73] op_sel_hi:[1,0,1]
	v_pk_fma_f32 v[74:75], v[90:91], v[162:163], v[74:75] op_sel_hi:[1,0,1]
	v_pk_fma_f32 v[76:77], v[92:93], v[162:163], v[76:77] op_sel_hi:[1,0,1]
	v_pk_fma_f32 v[78:79], v[94:95], v[162:163], v[78:79] op_sel_hi:[1,0,1]
	s_waitcnt lgkmcnt(1)
	v_mov_b32_e32 v182, v219
	v_pk_fma_f32 v[32:33], v[32:33], v[218:219], v[64:65] op_sel_hi:[1,0,1]
	v_pk_fma_f32 v[34:35], v[34:35], v[218:219], v[66:67] op_sel_hi:[1,0,1]
	v_pk_fma_f32 v[36:37], v[36:37], v[218:219], v[68:69] op_sel_hi:[1,0,1]
	v_pk_fma_f32 v[38:39], v[38:39], v[218:219], v[70:71] op_sel_hi:[1,0,1]
	v_pk_fma_f32 v[40:41], v[40:41], v[218:219], v[72:73] op_sel_hi:[1,0,1]
	v_pk_fma_f32 v[42:43], v[42:43], v[218:219], v[74:75] op_sel_hi:[1,0,1]
	v_pk_fma_f32 v[44:45], v[44:45], v[218:219], v[76:77] op_sel_hi:[1,0,1]
	v_pk_fma_f32 v[46:47], v[46:47], v[218:219], v[78:79] op_sel_hi:[1,0,1]
	v_cvt_scalef32_pk32_f32_fp6 v[0:31], v[222:227], 1.0
	v_pk_fma_f32 v[32:33], v[48:49], v[182:183], v[32:33] op_sel_hi:[1,0,1]
	v_pk_fma_f32 v[34:35], v[50:51], v[182:183], v[34:35] op_sel_hi:[1,0,1]
	v_pk_fma_f32 v[36:37], v[52:53], v[182:183], v[36:37] op_sel_hi:[1,0,1]
	v_pk_fma_f32 v[38:39], v[54:55], v[182:183], v[38:39] op_sel_hi:[1,0,1]
	v_pk_fma_f32 v[40:41], v[56:57], v[182:183], v[40:41] op_sel_hi:[1,0,1]
	v_pk_fma_f32 v[42:43], v[58:59], v[182:183], v[42:43] op_sel_hi:[1,0,1]
	v_pk_fma_f32 v[44:45], v[60:61], v[182:183], v[44:45] op_sel_hi:[1,0,1]
	v_pk_fma_f32 v[46:47], v[62:63], v[182:183], v[46:47] op_sel_hi:[1,0,1]
	s_waitcnt lgkmcnt(0)
; __device__ __forceinline__ int fresh_lane() { int l; asm volatile("v_mbcnt_lo_u32_b32 %0, -1, 0\n\tv_mbcnt_hi_u32_b32 %0, -1, %0" : "=v"(l)); return l; }
; __device__ __forceinline__ float bflo(unsigned w) { return __uint_as_float(w << 16); }
; __device__ __forceinline__ float bfhi(unsigned w) { return __uint_as_float(w & 0xffff0000u); }
; __device__ __forceinline__ float wave_sum(float v) { v = dpp_add16(v); return (rdlane(v, 0) + rdlane(v, 16)) + (rdlane(v, 32) + rdlane(v, 48)); }
; __device__ __forceinline__ void p12_peer(Frame& F) {
;     ...
;               float r8[8], r4[4];
; #pragma unroll
;               for (int m = 0; m < 8; ++m) { const float lo_v = (m & 1) ? acc2[m >> 1].y : acc2[m >> 1].x, hi_v = (m & 1) ? acc2[4 + (m >> 1)].y : acc2[4 + (m >> 1)].x;
;                   const float keep = hi5 ? hi_v : lo_v, send = hi5 ? lo_v : hi_v;
;                   r8[m] = keep + __builtin_bit_cast(float, __builtin_amdgcn_ds_bpermute((F.lane ^ 32) << 2, __builtin_bit_cast(int, send))); }
; #pragma unroll
;               for (int m = 0; m < 4; ++m) { const float keep = hi4 ? r8[4 + m] : r8[m], send = hi4 ? r8[m] : r8[4 + m];
;                   r4[m] = keep + __builtin_bit_cast(float, __builtin_amdgcn_ds_bpermute((F.lane ^ 16) << 2, __builtin_bit_cast(int, send))); }
;               int lo3_ = lo_; asm volatile("" : "+v"(lo3_));
;               const size_t col = (size_t)t * D_ + (size_t)(unsigned)(256 * c + lo3_);
;               const f32x4 o = {r4[0] + bflo(hb.x), r4[1] + bfhi(hb.x), r4[2] + bflo(hb.y), r4[3] + bfhi(hb.y)};
;               SSQ[i * 64 + F.lane] += (o.x * o.x + o.y * o.y) + (o.z * o.z + o.w * o.w);
;               *(f32x4*)(F.out + col) = o;
;     ...
;       __builtin_amdgcn_fence(__ATOMIC_SEQ_CST, "agent");
;       const int l2_ = fresh_lane(), lo2_ = 16 * (l2_ & 15) + 4 * (l2_ >> 4);
; #pragma unroll
;       for (int i = 0; i < 4; ++i) { const int t = F.gw + i * F.NGW;
;           const float rs = 1.0f / sqrtf(wave_sum(SSQ[i * 64 + l2_]) * (1.f / D_) + 1e-6f);
; _Pragma("nounroll")
;           for (int c0 = 0; c0 < 16; c0 += 8) {
; #pragma unroll
;               for (int c = c0; c < c0 + 8; ++c) { const size_t col = (size_t)t * D_ + (size_t)(unsigned)(256 * c + lo2_); const f32x4 gn = *(const f32x4*)(lnf + (256 * c + lo2_));
;                   const f32x4 o = *(const f32x4*)(F.out + col);
	v_mov_b32_e32 v184, v221
	v_pk_fma_f32 v[0:1], v[0:1], v[220:221], v[32:33] op_sel_hi:[1,0,1]
	v_pk_fma_f32 v[2:3], v[2:3], v[220:221], v[34:35] op_sel_hi:[1,0,1]
	v_pk_fma_f32 v[4:5], v[4:5], v[220:221], v[36:37] op_sel_hi:[1,0,1]
	v_pk_fma_f32 v[6:7], v[6:7], v[220:221], v[38:39] op_sel_hi:[1,0,1]
	v_pk_fma_f32 v[8:9], v[8:9], v[220:221], v[40:41] op_sel_hi:[1,0,1]
	v_pk_fma_f32 v[10:11], v[10:11], v[220:221], v[42:43] op_sel_hi:[1,0,1]
	v_pk_fma_f32 v[12:13], v[12:13], v[220:221], v[44:45] op_sel_hi:[1,0,1]
	v_pk_fma_f32 v[14:15], v[14:15], v[220:221], v[46:47] op_sel_hi:[1,0,1]
	v_pk_fma_f32 v[0:1], v[16:17], v[184:185], v[0:1] op_sel_hi:[1,0,1]
	v_pk_fma_f32 v[2:3], v[18:19], v[184:185], v[2:3] op_sel_hi:[1,0,1]
	v_pk_fma_f32 v[4:5], v[20:21], v[184:185], v[4:5] op_sel_hi:[1,0,1]
	v_pk_fma_f32 v[6:7], v[22:23], v[184:185], v[6:7] op_sel_hi:[1,0,1]
	v_pk_fma_f32 v[8:9], v[24:25], v[184:185], v[8:9] op_sel_hi:[1,0,1]
	v_pk_fma_f32 v[10:11], v[26:27], v[184:185], v[10:11] op_sel_hi:[1,0,1]
	v_pk_fma_f32 v[12:13], v[28:29], v[184:185], v[12:13] op_sel_hi:[1,0,1]
	v_pk_fma_f32 v[14:15], v[30:31], v[184:185], v[14:15] op_sel_hi:[1,0,1]
	v_cndmask_b32_e32 v18, v0, v8, vcc
	v_cndmask_b32_e32 v19, v1, v9, vcc
	v_cndmask_b32_e32 v20, v2, v10, vcc
	v_cndmask_b32_e32 v21, v3, v11, vcc
	v_cndmask_b32_e32 v22, v4, v12, vcc
	v_cndmask_b32_e32 v23, v5, v13, vcc
	v_cndmask_b32_e32 v24, v6, v14, vcc
	v_cndmask_b32_e32 v25, v7, v15, vcc
	v_cndmask_b32_e32 v17, v10, v2, vcc
	v_cndmask_b32_e32 v16, v8, v0, vcc
	v_cndmask_b32_e32 v3, v11, v3, vcc
	v_cndmask_b32_e32 v2, v9, v1, vcc
	v_cndmask_b32_e32 v1, v14, v6, vcc
	v_cndmask_b32_e32 v0, v12, v4, vcc
	v_cndmask_b32_e32 v6, v13, v5, vcc
	ds_bpermute_b32 v4, v171, v18
	ds_bpermute_b32 v8, v171, v19
	ds_bpermute_b32 v5, v171, v20
	ds_bpermute_b32 v9, v171, v21
	ds_bpermute_b32 v10, v171, v22
	ds_bpermute_b32 v12, v171, v23
	ds_bpermute_b32 v11, v171, v24
	ds_bpermute_b32 v13, v171, v25
	v_cndmask_b32_e32 v7, v15, v7, vcc
	s_waitcnt lgkmcnt(5)
	v_pk_add_f32 v[4:5], v[16:17], v[4:5]
	s_waitcnt lgkmcnt(4)
	v_pk_add_f32 v[2:3], v[2:3], v[8:9]
	s_waitcnt lgkmcnt(1)
	v_pk_add_f32 v[0:1], v[0:1], v[10:11]
	s_waitcnt lgkmcnt(0)
	v_pk_add_f32 v[6:7], v[6:7], v[12:13]
	v_cndmask_b32_e64 v10, v4, v0, s[0:1]
	v_cndmask_b32_e64 v11, v2, v6, s[0:1]
	v_cndmask_b32_e64 v9, v1, v5, s[0:1]
	v_cndmask_b32_e64 v8, v0, v4, s[0:1]
	v_cndmask_b32_e64 v5, v5, v1, s[0:1]
	v_cndmask_b32_e64 v0, v6, v2, s[0:1]
	v_cndmask_b32_e64 v6, v3, v7, s[0:1]
	v_cndmask_b32_e64 v1, v7, v3, s[0:1]
	ds_bpermute_b32 v2, v170, v10
	ds_bpermute_b32 v4, v170, v11
	ds_bpermute_b32 v3, v170, v5
	ds_bpermute_b32 v5, v170, v6
	v_add_u32_e32 v178, s28, v174
	ds_read_b32 v155, v178
	s_addk_i32 s28, 0x100
	s_waitcnt lgkmcnt(2)
	v_pk_add_f32 v[2:3], v[8:9], v[2:3]
	s_waitcnt lgkmcnt(1)
	v_pk_add_f32 v[0:1], v[0:1], v[4:5]
	v_pk_add_f32 v[4:5], v[2:3], v[166:167]
	v_pk_add_f32 v[2:3], v[0:1], v[168:169]
	v_mov_b32_e32 v0, v4
	v_pk_mul_f32 v[6:7], v[2:3], v[2:3]
	v_mov_b32_e32 v1, v2
	v_mov_b32_e32 v2, v5
	v_pk_fma_f32 v[4:5], v[4:5], v[4:5], v[6:7]
	s_addk_i32 s23, 0x80
	s_add_i32 s12, s12, s34
	global_store_dwordx4 v[180:181], v[0:3], off nt
	s_cmpk_eq_i32 s28, 0x400
	v_add_u32_e32 v177, 0x200, v177
	v_add_f32_e32 v0, v4, v5
	s_waitcnt vmcnt(1)
	v_mov_b32_e32 v149, v202
	v_mov_b32_e32 v150, v203
	v_mov_b32_e32 v151, v204
	v_mov_b32_e32 v143, v198
	v_mov_b32_e32 v144, v199
	v_mov_b32_e32 v145, v200
	v_mov_b32_e32 v131, v156
	v_mov_b32_e32 v132, v157
	v_mov_b32_e32 v133, v158
	v_mov_b32_e32 v137, v152
	v_mov_b32_e32 v138, v153
	v_mov_b32_e32 v139, v154
	s_waitcnt lgkmcnt(0)
	v_add_f32_e32 v0, v155, v0
	ds_write_b32 v178, v0
	s_cbranch_scc0 .LBB0_3403
	s_cmp_eq_u32 s19, 16
	s_mov_b32 s17, s19
	s_cbranch_scc0 .LBB0_3402
	s_waitcnt vmcnt(0) lgkmcnt(0)
	buffer_inv sc1
	v_mbcnt_lo_u32_b32 v0, -1, 0
	v_mbcnt_hi_u32_b32 v0, -1, v0
	v_lshl_add_u32 v7, v0, 2, s20
	v_and_b32_e32 v2, 15, v0
	v_lshrrev_b32_e32 v3, 4, v0
	v_lshlrev_b32_e32 v2, 6, v2
	v_lshl_add_u32 v6, v3, 4, v2
	v_add_u32_e32 v10, 0x1000, v6
	v_add_u32_e32 v11, 0x2000, v6
	v_add_u32_e32 v12, 0x3000, v6
	s_lshl_b64 s[0:1], s[94:95], 14
	s_add_u32 s12, s26, s0
	s_addc_u32 s13, s27, s1
	s_lshl_b64 s[0:1], s[4:5], 14
	s_add_u32 s14, s26, s0
	s_addc_u32 s15, s27, s1
	s_lshl_b64 s[0:1], s[8:9], 14
	s_add_u32 s16, s26, s0
	s_addc_u32 s17, s27, s1
	s_lshl_b64 s[0:1], s[10:11], 14
	s_add_u32 s18, s26, s0
	s_addc_u32 s19, s27, s1
	global_load_dwordx4 v[60:63], v6, s[24:25] offset:0
	global_load_dwordx4 v[64:67], v6, s[24:25] offset:1024
	global_load_dwordx4 v[68:71], v6, s[24:25] offset:2048
	global_load_dwordx4 v[72:75], v6, s[24:25] offset:3072
	global_load_dwordx4 v[76:79], v10, s[24:25] offset:0
	global_load_dwordx4 v[80:83], v10, s[24:25] offset:1024
	global_load_dwordx4 v[84:87], v10, s[24:25] offset:2048
	global_load_dwordx4 v[88:91], v10, s[24:25] offset:3072
	global_load_dwordx4 v[92:95], v11, s[24:25] offset:0
	global_load_dwordx4 v[96:99], v11, s[24:25] offset:1024
	global_load_dwordx4 v[100:103], v11, s[24:25] offset:2048
	global_load_dwordx4 v[104:107], v11, s[24:25] offset:3072
	global_load_dwordx4 v[108:111], v12, s[24:25] offset:0
	global_load_dwordx4 v[112:115], v12, s[24:25] offset:1024
	global_load_dwordx4 v[116:119], v12, s[24:25] offset:2048
	global_load_dwordx4 v[120:123], v12, s[24:25] offset:3072
	global_load_dwordx4 v[124:127], v6, s[12:13] offset:0
	global_load_dwordx4 v[128:131], v6, s[12:13] offset:1024
	global_load_dwordx4 v[132:135], v6, s[12:13] offset:2048
	global_load_dwordx4 v[136:139], v6, s[12:13] offset:3072
	global_load_dwordx4 v[140:143], v10, s[12:13] offset:0
; __device__ __forceinline__ float wave_sum(float v) { v = dpp_add16(v); return (rdlane(v, 0) + rdlane(v, 16)) + (rdlane(v, 32) + rdlane(v, 48)); }
; __device__ __forceinline__ void p12_peer(Frame& F) {
;     ...
;       for (int i = 0; i < 4; ++i) { const int t = F.gw + i * F.NGW;
;           const float rs = 1.0f / sqrtf(wave_sum(SSQ[i * 64 + l2_]) * (1.f / D_) + 1e-6f);
; _Pragma("nounroll")
;           for (int c0 = 0; c0 < 16; c0 += 8) {
; #pragma unroll
;               for (int c = c0; c < c0 + 8; ++c) { const size_t col = (size_t)t * D_ + (size_t)(unsigned)(256 * c + lo2_); const f32x4 gn = *(const f32x4*)(lnf + (256 * c + lo2_));
;                   const f32x4 o = *(const f32x4*)(F.out + col);
	global_load_dwordx4 v[144:147], v10, s[12:13] offset:1024
	global_load_dwordx4 v[148:151], v10, s[12:13] offset:2048
	global_load_dwordx4 v[152:155], v10, s[12:13] offset:3072
	global_load_dwordx4 v[156:159], v11, s[12:13] offset:0
	global_load_dwordx4 v[160:163], v11, s[12:13] offset:1024
	global_load_dwordx4 v[164:167], v11, s[12:13] offset:2048
	global_load_dwordx4 v[168:171], v11, s[12:13] offset:3072
	global_load_dwordx4 v[172:175], v12, s[12:13] offset:0
	global_load_dwordx4 v[176:179], v12, s[12:13] offset:1024
	global_load_dwordx4 v[180:183], v12, s[12:13] offset:2048
	global_load_dwordx4 v[184:187], v12, s[12:13] offset:3072
	global_load_dwordx4 v[188:191], v6, s[14:15] offset:0
	global_load_dwordx4 v[192:195], v6, s[14:15] offset:1024
	global_load_dwordx4 v[196:199], v6, s[14:15] offset:2048
	global_load_dwordx4 v[200:203], v6, s[14:15] offset:3072
	global_load_dwordx4 v[204:207], v10, s[14:15] offset:0
	global_load_dwordx4 v[208:211], v10, s[14:15] offset:1024
	global_load_dwordx4 v[212:215], v10, s[14:15] offset:2048
	global_load_dwordx4 v[216:219], v10, s[14:15] offset:3072
	global_load_dwordx4 v[220:223], v11, s[14:15] offset:0
	global_load_dwordx4 v[224:227], v11, s[14:15] offset:1024
	global_load_dwordx4 v[228:231], v11, s[14:15] offset:2048
	global_load_dwordx4 v[232:235], v11, s[14:15] offset:3072
	global_load_dwordx4 v[236:239], v12, s[14:15] offset:0
	global_load_dwordx4 v[240:243], v12, s[14:15] offset:1024
	global_load_dwordx4 v[244:247], v12, s[14:15] offset:2048
	global_load_dwordx4 v[248:251], v12, s[14:15] offset:3072
	ds_read_b32 v1, v7 offset:4096
	s_waitcnt lgkmcnt(0)
	v_add_f32_dpp v1, v1, v1 quad_perm:[1,0,3,2] row_mask:0xf bank_mask:0xf bound_ctrl:1
	s_nop 1
	v_add_f32_dpp v1, v1, v1 quad_perm:[2,3,0,1] row_mask:0xf bank_mask:0xf bound_ctrl:1
	s_nop 1
	v_add_f32_dpp v1, v1, v1 row_half_mirror row_mask:0xf bank_mask:0xf bound_ctrl:1
	s_nop 1
	v_add_f32_dpp v1, v1, v1 row_mirror row_mask:0xf bank_mask:0xf bound_ctrl:1
	s_nop 0
	v_readlane_b32 s1, v1, 16
	v_readlane_b32 s0, v1, 0
	s_nop 0
	v_mov_b32_e32 v3, s1
	v_readlane_b32 s1, v1, 48
	v_add_f32_e32 v3, s0, v3
	v_readlane_b32 s0, v1, 32
	v_mov_b32_e32 v1, s1
	s_nop 0
	v_add_f32_e32 v1, s0, v1
	v_add_f32_e32 v1, v3, v1
	v_mov_b32_e32 v3, 0x358637bd
	v_fmac_f32_e32 v3, 0x39800000, v1
	s_mov_b32 s0, 0xf800000
	v_mul_f32_e32 v1, 0x4f800000, v3
	v_cmp_gt_f32_e32 vcc, s0, v3
	s_nop 1
	v_cndmask_b32_e32 v1, v3, v1, vcc
	v_sqrt_f32_e32 v3, v1
	s_nop 0
	v_add_u32_e32 v4, -1, v3
	v_fma_f32 v5, -v4, v3, v1
	v_cmp_ge_f32_e64 s[0:1], 0, v5
	v_add_u32_e32 v5, 1, v3
	s_nop 0
	v_cndmask_b32_e64 v4, v3, v4, s[0:1]
	v_fma_f32 v3, -v5, v3, v1
	v_cmp_lt_f32_e64 s[0:1], 0, v3
	s_nop 1
	v_cndmask_b32_e64 v3, v4, v5, s[0:1]
	v_mul_f32_e32 v4, 0x37800000, v3
	v_cndmask_b32_e32 v3, v3, v4, vcc
	v_mov_b32_e32 v4, 0x260
	v_cmp_class_f32_e32 vcc, v1, v4
	s_nop 1
	v_cndmask_b32_e32 v3, v3, v1, vcc
	v_div_scale_f32 v4, s[0:1], v3, v3, 1.0
	v_rcp_f32_e32 v5, v4
	s_nop 0
	v_fma_f32 v0, -v4, v5, 1.0
	v_fmac_f32_e32 v5, v0, v5
	v_div_scale_f32 v0, vcc, 1.0, v3, 1.0
	v_mul_f32_e32 v2, v0, v5
	v_fma_f32 v8, -v4, v2, v0
	v_fmac_f32_e32 v2, v8, v5
	v_fma_f32 v0, -v4, v2, v0
	v_div_fmas_f32 v0, v0, v5, v2
	v_div_fixup_f32 v2, v0, v3, 1.0
	v_mov_b32_e32 v40, v2
	v_mov_b32_e32 v41, v2
	ds_read_b32 v1, v7 offset:4352
	s_waitcnt lgkmcnt(0)
	v_add_f32_dpp v1, v1, v1 quad_perm:[1,0,3,2] row_mask:0xf bank_mask:0xf bound_ctrl:1
	s_nop 1
	v_add_f32_dpp v1, v1, v1 quad_perm:[2,3,0,1] row_mask:0xf bank_mask:0xf bound_ctrl:1
	s_nop 1
	v_add_f32_dpp v1, v1, v1 row_half_mirror row_mask:0xf bank_mask:0xf bound_ctrl:1
	s_nop 1
	v_add_f32_dpp v1, v1, v1 row_mirror row_mask:0xf bank_mask:0xf bound_ctrl:1
	s_nop 0
	v_readlane_b32 s1, v1, 16
	v_readlane_b32 s0, v1, 0
	s_nop 0
	v_mov_b32_e32 v3, s1
	v_readlane_b32 s1, v1, 48
	v_add_f32_e32 v3, s0, v3
	v_readlane_b32 s0, v1, 32
	v_mov_b32_e32 v1, s1
	s_nop 0
	v_add_f32_e32 v1, s0, v1
	v_add_f32_e32 v1, v3, v1
	v_mov_b32_e32 v3, 0x358637bd
	v_fmac_f32_e32 v3, 0x39800000, v1
	s_mov_b32 s0, 0xf800000
	v_mul_f32_e32 v1, 0x4f800000, v3
	v_cmp_gt_f32_e32 vcc, s0, v3
	s_nop 1
	v_cndmask_b32_e32 v1, v3, v1, vcc
	v_sqrt_f32_e32 v3, v1
	s_nop 0
	v_add_u32_e32 v4, -1, v3
	v_fma_f32 v5, -v4, v3, v1
	v_cmp_ge_f32_e64 s[0:1], 0, v5
	v_add_u32_e32 v5, 1, v3
	s_nop 0
	v_cndmask_b32_e64 v4, v3, v4, s[0:1]
	v_fma_f32 v3, -v5, v3, v1
	v_cmp_lt_f32_e64 s[0:1], 0, v3
	s_nop 1
	v_cndmask_b32_e64 v3, v4, v5, s[0:1]
	v_mul_f32_e32 v4, 0x37800000, v3
	v_cndmask_b32_e32 v3, v3, v4, vcc
	v_mov_b32_e32 v4, 0x260
	v_cmp_class_f32_e32 vcc, v1, v4
	s_nop 1
	v_cndmask_b32_e32 v3, v3, v1, vcc
	v_div_scale_f32 v4, s[0:1], v3, v3, 1.0
	v_rcp_f32_e32 v5, v4
	s_nop 0
	v_fma_f32 v0, -v4, v5, 1.0
	v_fmac_f32_e32 v5, v0, v5
	v_div_scale_f32 v0, vcc, 1.0, v3, 1.0
	v_mul_f32_e32 v2, v0, v5
	v_fma_f32 v8, -v4, v2, v0
	v_fmac_f32_e32 v2, v8, v5
	v_fma_f32 v0, -v4, v2, v0
	v_div_fmas_f32 v0, v0, v5, v2
	v_div_fixup_f32 v2, v0, v3, 1.0
	v_mov_b32_e32 v42, v2
	v_mov_b32_e32 v43, v2
	ds_read_b32 v1, v7 offset:4608
	s_waitcnt lgkmcnt(0)
; __device__ __forceinline__ float wave_sum(float v) { v = dpp_add16(v); return (rdlane(v, 0) + rdlane(v, 16)) + (rdlane(v, 32) + rdlane(v, 48)); }
; __device__ __forceinline__ void p12_peer(Frame& F) {
;     ...
;       for (int i = 0; i < 4; ++i) { const int t = F.gw + i * F.NGW;
;           const float rs = 1.0f / sqrtf(wave_sum(SSQ[i * 64 + l2_]) * (1.f / D_) + 1e-6f);
; _Pragma("nounroll")
;           for (int c0 = 0; c0 < 16; c0 += 8) {
; #pragma unroll
;               for (int c = c0; c < c0 + 8; ++c) { const size_t col = (size_t)t * D_ + (size_t)(unsigned)(256 * c + lo2_); const f32x4 gn = *(const f32x4*)(lnf + (256 * c + lo2_));
;                   const f32x4 o = *(const f32x4*)(F.out + col);
;                   *(f32x4*)(F.out + col) = (f32x4){o.x * rs * gn.x, o.y * rs * gn.y, o.z * rs * gn.z, o.w * rs * gn.w}; }
	v_add_f32_dpp v1, v1, v1 quad_perm:[1,0,3,2] row_mask:0xf bank_mask:0xf bound_ctrl:1
	s_nop 1
	v_add_f32_dpp v1, v1, v1 quad_perm:[2,3,0,1] row_mask:0xf bank_mask:0xf bound_ctrl:1
	s_nop 1
	v_add_f32_dpp v1, v1, v1 row_half_mirror row_mask:0xf bank_mask:0xf bound_ctrl:1
	s_nop 1
	v_add_f32_dpp v1, v1, v1 row_mirror row_mask:0xf bank_mask:0xf bound_ctrl:1
	s_nop 0
	v_readlane_b32 s1, v1, 16
	v_readlane_b32 s0, v1, 0
	s_nop 0
	v_mov_b32_e32 v3, s1
	v_readlane_b32 s1, v1, 48
	v_add_f32_e32 v3, s0, v3
	v_readlane_b32 s0, v1, 32
	v_mov_b32_e32 v1, s1
	s_nop 0
	v_add_f32_e32 v1, s0, v1
	v_add_f32_e32 v1, v3, v1
	v_mov_b32_e32 v3, 0x358637bd
	v_fmac_f32_e32 v3, 0x39800000, v1
	s_mov_b32 s0, 0xf800000
	v_mul_f32_e32 v1, 0x4f800000, v3
	v_cmp_gt_f32_e32 vcc, s0, v3
	s_nop 1
	v_cndmask_b32_e32 v1, v3, v1, vcc
	v_sqrt_f32_e32 v3, v1
	s_nop 0
	v_add_u32_e32 v4, -1, v3
	v_fma_f32 v5, -v4, v3, v1
	v_cmp_ge_f32_e64 s[0:1], 0, v5
	v_add_u32_e32 v5, 1, v3
	s_nop 0
	v_cndmask_b32_e64 v4, v3, v4, s[0:1]
	v_fma_f32 v3, -v5, v3, v1
	v_cmp_lt_f32_e64 s[0:1], 0, v3
	s_nop 1
	v_cndmask_b32_e64 v3, v4, v5, s[0:1]
	v_mul_f32_e32 v4, 0x37800000, v3
	v_cndmask_b32_e32 v3, v3, v4, vcc
	v_mov_b32_e32 v4, 0x260
	v_cmp_class_f32_e32 vcc, v1, v4
	s_nop 1
	v_cndmask_b32_e32 v3, v3, v1, vcc
	v_div_scale_f32 v4, s[0:1], v3, v3, 1.0
	v_rcp_f32_e32 v5, v4
	s_nop 0
	v_fma_f32 v0, -v4, v5, 1.0
	v_fmac_f32_e32 v5, v0, v5
	v_div_scale_f32 v0, vcc, 1.0, v3, 1.0
	v_mul_f32_e32 v2, v0, v5
	v_fma_f32 v8, -v4, v2, v0
	v_fmac_f32_e32 v2, v8, v5
	v_fma_f32 v0, -v4, v2, v0
	v_div_fmas_f32 v0, v0, v5, v2
	v_div_fixup_f32 v2, v0, v3, 1.0
	v_mov_b32_e32 v44, v2
	v_mov_b32_e32 v45, v2
	ds_read_b32 v1, v7 offset:4864
	s_waitcnt lgkmcnt(0)
	v_add_f32_dpp v1, v1, v1 quad_perm:[1,0,3,2] row_mask:0xf bank_mask:0xf bound_ctrl:1
	s_nop 1
	v_add_f32_dpp v1, v1, v1 quad_perm:[2,3,0,1] row_mask:0xf bank_mask:0xf bound_ctrl:1
	s_nop 1
	v_add_f32_dpp v1, v1, v1 row_half_mirror row_mask:0xf bank_mask:0xf bound_ctrl:1
	s_nop 1
	v_add_f32_dpp v1, v1, v1 row_mirror row_mask:0xf bank_mask:0xf bound_ctrl:1
	s_nop 0
	v_readlane_b32 s1, v1, 16
	v_readlane_b32 s0, v1, 0
	s_nop 0
	v_mov_b32_e32 v3, s1
	v_readlane_b32 s1, v1, 48
	v_add_f32_e32 v3, s0, v3
	v_readlane_b32 s0, v1, 32
	v_mov_b32_e32 v1, s1
	s_nop 0
	v_add_f32_e32 v1, s0, v1
	v_add_f32_e32 v1, v3, v1
	v_mov_b32_e32 v3, 0x358637bd
	v_fmac_f32_e32 v3, 0x39800000, v1
	s_mov_b32 s0, 0xf800000
	v_mul_f32_e32 v1, 0x4f800000, v3
	v_cmp_gt_f32_e32 vcc, s0, v3
	s_nop 1
	v_cndmask_b32_e32 v1, v3, v1, vcc
	v_sqrt_f32_e32 v3, v1
	s_nop 0
	v_add_u32_e32 v4, -1, v3
	v_fma_f32 v5, -v4, v3, v1
	v_cmp_ge_f32_e64 s[0:1], 0, v5
	v_add_u32_e32 v5, 1, v3
	s_nop 0
	v_cndmask_b32_e64 v4, v3, v4, s[0:1]
	v_fma_f32 v3, -v5, v3, v1
	v_cmp_lt_f32_e64 s[0:1], 0, v3
	s_nop 1
	v_cndmask_b32_e64 v3, v4, v5, s[0:1]
	v_mul_f32_e32 v4, 0x37800000, v3
	v_cndmask_b32_e32 v3, v3, v4, vcc
	v_mov_b32_e32 v4, 0x260
	v_cmp_class_f32_e32 vcc, v1, v4
	s_nop 1
	v_cndmask_b32_e32 v3, v3, v1, vcc
	v_div_scale_f32 v4, s[0:1], v3, v3, 1.0
	v_rcp_f32_e32 v5, v4
	s_nop 0
	v_fma_f32 v0, -v4, v5, 1.0
	v_fmac_f32_e32 v5, v0, v5
	v_div_scale_f32 v0, vcc, 1.0, v3, 1.0
	v_mul_f32_e32 v2, v0, v5
	v_fma_f32 v8, -v4, v2, v0
	v_fmac_f32_e32 v2, v8, v5
	v_fma_f32 v0, -v4, v2, v0
	v_div_fmas_f32 v0, v0, v5, v2
	v_div_fixup_f32 v2, v0, v3, 1.0
	v_mov_b32_e32 v46, v2
	v_mov_b32_e32 v47, v2
	s_waitcnt vmcnt(31)
	v_pk_mul_f32 v[124:125], v[40:41], v[124:125]
	v_pk_mul_f32 v[126:127], v[40:41], v[126:127]
	v_pk_mul_f32 v[124:125], v[60:61], v[124:125]
	v_pk_mul_f32 v[126:127], v[62:63], v[126:127]
	global_store_dwordx4 v6, v[124:127], s[12:13] offset:0
	s_waitcnt vmcnt(31)
	v_pk_mul_f32 v[128:129], v[40:41], v[128:129]
	v_pk_mul_f32 v[130:131], v[40:41], v[130:131]
	v_pk_mul_f32 v[128:129], v[64:65], v[128:129]
	v_pk_mul_f32 v[130:131], v[66:67], v[130:131]
	global_store_dwordx4 v6, v[128:131], s[12:13] offset:1024
	s_waitcnt vmcnt(31)
	v_pk_mul_f32 v[132:133], v[40:41], v[132:133]
	v_pk_mul_f32 v[134:135], v[40:41], v[134:135]
	v_pk_mul_f32 v[132:133], v[68:69], v[132:133]
	v_pk_mul_f32 v[134:135], v[70:71], v[134:135]
	global_store_dwordx4 v6, v[132:135], s[12:13] offset:2048
	s_waitcnt vmcnt(31)
	v_pk_mul_f32 v[136:137], v[40:41], v[136:137]
	v_pk_mul_f32 v[138:139], v[40:41], v[138:139]
	v_pk_mul_f32 v[136:137], v[72:73], v[136:137]
	v_pk_mul_f32 v[138:139], v[74:75], v[138:139]
	global_store_dwordx4 v6, v[136:139], s[12:13] offset:3072
	s_waitcnt vmcnt(31)
	v_pk_mul_f32 v[140:141], v[40:41], v[140:141]
	v_pk_mul_f32 v[142:143], v[40:41], v[142:143]
	v_pk_mul_f32 v[140:141], v[76:77], v[140:141]
	v_pk_mul_f32 v[142:143], v[78:79], v[142:143]
	global_store_dwordx4 v10, v[140:143], s[12:13] offset:0
	s_waitcnt vmcnt(31)
	v_pk_mul_f32 v[144:145], v[40:41], v[144:145]
	v_pk_mul_f32 v[146:147], v[40:41], v[146:147]
	v_pk_mul_f32 v[144:145], v[80:81], v[144:145]
	v_pk_mul_f32 v[146:147], v[82:83], v[146:147]
	global_store_dwordx4 v10, v[144:147], s[12:13] offset:1024
	s_waitcnt vmcnt(31)
	v_pk_mul_f32 v[148:149], v[40:41], v[148:149]
	v_pk_mul_f32 v[150:151], v[40:41], v[150:151]
	v_pk_mul_f32 v[148:149], v[84:85], v[148:149]
	v_pk_mul_f32 v[150:151], v[86:87], v[150:151]
	global_store_dwordx4 v10, v[148:151], s[12:13] offset:2048
	s_waitcnt vmcnt(31)
	v_pk_mul_f32 v[152:153], v[40:41], v[152:153]
	v_pk_mul_f32 v[154:155], v[40:41], v[154:155]
	v_pk_mul_f32 v[152:153], v[88:89], v[152:153]
	v_pk_mul_f32 v[154:155], v[90:91], v[154:155]
	global_store_dwordx4 v10, v[152:155], s[12:13] offset:3072
	s_waitcnt vmcnt(31)
; __device__ __forceinline__ void p12_peer(Frame& F) {
;     ...
; #pragma unroll
;               for (int c = c0; c < c0 + 8; ++c) { const size_t col = (size_t)t * D_ + (size_t)(unsigned)(256 * c + lo2_); const f32x4 gn = *(const f32x4*)(lnf + (256 * c + lo2_));
;                   const f32x4 o = *(const f32x4*)(F.out + col);
;                   *(f32x4*)(F.out + col) = (f32x4){o.x * rs * gn.x, o.y * rs * gn.y, o.z * rs * gn.z, o.w * rs * gn.w}; }
	v_pk_mul_f32 v[156:157], v[40:41], v[156:157]
	v_pk_mul_f32 v[158:159], v[40:41], v[158:159]
	v_pk_mul_f32 v[156:157], v[92:93], v[156:157]
	v_pk_mul_f32 v[158:159], v[94:95], v[158:159]
	global_store_dwordx4 v11, v[156:159], s[12:13] offset:0
	s_waitcnt vmcnt(31)
	v_pk_mul_f32 v[160:161], v[40:41], v[160:161]
	v_pk_mul_f32 v[162:163], v[40:41], v[162:163]
	v_pk_mul_f32 v[160:161], v[96:97], v[160:161]
	v_pk_mul_f32 v[162:163], v[98:99], v[162:163]
	global_store_dwordx4 v11, v[160:163], s[12:13] offset:1024
	s_waitcnt vmcnt(31)
	v_pk_mul_f32 v[164:165], v[40:41], v[164:165]
	v_pk_mul_f32 v[166:167], v[40:41], v[166:167]
	v_pk_mul_f32 v[164:165], v[100:101], v[164:165]
	v_pk_mul_f32 v[166:167], v[102:103], v[166:167]
	global_store_dwordx4 v11, v[164:167], s[12:13] offset:2048
	s_waitcnt vmcnt(31)
	v_pk_mul_f32 v[168:169], v[40:41], v[168:169]
	v_pk_mul_f32 v[170:171], v[40:41], v[170:171]
	v_pk_mul_f32 v[168:169], v[104:105], v[168:169]
	v_pk_mul_f32 v[170:171], v[106:107], v[170:171]
	global_store_dwordx4 v11, v[168:171], s[12:13] offset:3072
	s_waitcnt vmcnt(31)
	v_pk_mul_f32 v[172:173], v[40:41], v[172:173]
	v_pk_mul_f32 v[174:175], v[40:41], v[174:175]
	v_pk_mul_f32 v[172:173], v[108:109], v[172:173]
	v_pk_mul_f32 v[174:175], v[110:111], v[174:175]
	global_store_dwordx4 v12, v[172:175], s[12:13] offset:0
	s_waitcnt vmcnt(31)
	v_pk_mul_f32 v[176:177], v[40:41], v[176:177]
	v_pk_mul_f32 v[178:179], v[40:41], v[178:179]
	v_pk_mul_f32 v[176:177], v[112:113], v[176:177]
	v_pk_mul_f32 v[178:179], v[114:115], v[178:179]
	global_store_dwordx4 v12, v[176:179], s[12:13] offset:1024
	s_waitcnt vmcnt(31)
	v_pk_mul_f32 v[180:181], v[40:41], v[180:181]
	v_pk_mul_f32 v[182:183], v[40:41], v[182:183]
	v_pk_mul_f32 v[180:181], v[116:117], v[180:181]
	v_pk_mul_f32 v[182:183], v[118:119], v[182:183]
	global_store_dwordx4 v12, v[180:183], s[12:13] offset:2048
	s_waitcnt vmcnt(31)
	v_pk_mul_f32 v[184:185], v[40:41], v[184:185]
	v_pk_mul_f32 v[186:187], v[40:41], v[186:187]
	v_pk_mul_f32 v[184:185], v[120:121], v[184:185]
	v_pk_mul_f32 v[186:187], v[122:123], v[186:187]
	global_store_dwordx4 v12, v[184:187], s[12:13] offset:3072
	s_nop 1
	global_load_dwordx4 v[124:127], v6, s[16:17] offset:0
	global_load_dwordx4 v[128:131], v6, s[16:17] offset:1024
	global_load_dwordx4 v[132:135], v6, s[16:17] offset:2048
	global_load_dwordx4 v[136:139], v6, s[16:17] offset:3072
	global_load_dwordx4 v[140:143], v10, s[16:17] offset:0
	global_load_dwordx4 v[144:147], v10, s[16:17] offset:1024
	global_load_dwordx4 v[148:151], v10, s[16:17] offset:2048
	global_load_dwordx4 v[152:155], v10, s[16:17] offset:3072
	global_load_dwordx4 v[156:159], v11, s[16:17] offset:0
	global_load_dwordx4 v[160:163], v11, s[16:17] offset:1024
	global_load_dwordx4 v[164:167], v11, s[16:17] offset:2048
	global_load_dwordx4 v[168:171], v11, s[16:17] offset:3072
	global_load_dwordx4 v[172:175], v12, s[16:17] offset:0
	global_load_dwordx4 v[176:179], v12, s[16:17] offset:1024
	global_load_dwordx4 v[180:183], v12, s[16:17] offset:2048
	global_load_dwordx4 v[184:187], v12, s[16:17] offset:3072
	s_waitcnt vmcnt(47)
	v_pk_mul_f32 v[188:189], v[42:43], v[188:189]
	v_pk_mul_f32 v[190:191], v[42:43], v[190:191]
	v_pk_mul_f32 v[188:189], v[60:61], v[188:189]
	v_pk_mul_f32 v[190:191], v[62:63], v[190:191]
	global_store_dwordx4 v6, v[188:191], s[14:15] offset:0
	s_waitcnt vmcnt(47)
	v_pk_mul_f32 v[192:193], v[42:43], v[192:193]
	v_pk_mul_f32 v[194:195], v[42:43], v[194:195]
	v_pk_mul_f32 v[192:193], v[64:65], v[192:193]
	v_pk_mul_f32 v[194:195], v[66:67], v[194:195]
	global_store_dwordx4 v6, v[192:195], s[14:15] offset:1024
	s_waitcnt vmcnt(47)
	v_pk_mul_f32 v[196:197], v[42:43], v[196:197]
	v_pk_mul_f32 v[198:199], v[42:43], v[198:199]
	v_pk_mul_f32 v[196:197], v[68:69], v[196:197]
	v_pk_mul_f32 v[198:199], v[70:71], v[198:199]
	global_store_dwordx4 v6, v[196:199], s[14:15] offset:2048
	s_waitcnt vmcnt(47)
	v_pk_mul_f32 v[200:201], v[42:43], v[200:201]
	v_pk_mul_f32 v[202:203], v[42:43], v[202:203]
	v_pk_mul_f32 v[200:201], v[72:73], v[200:201]
	v_pk_mul_f32 v[202:203], v[74:75], v[202:203]
	global_store_dwordx4 v6, v[200:203], s[14:15] offset:3072
	s_waitcnt vmcnt(47)
	v_pk_mul_f32 v[204:205], v[42:43], v[204:205]
	v_pk_mul_f32 v[206:207], v[42:43], v[206:207]
	v_pk_mul_f32 v[204:205], v[76:77], v[204:205]
	v_pk_mul_f32 v[206:207], v[78:79], v[206:207]
	global_store_dwordx4 v10, v[204:207], s[14:15] offset:0
	s_waitcnt vmcnt(47)
	v_pk_mul_f32 v[208:209], v[42:43], v[208:209]
	v_pk_mul_f32 v[210:211], v[42:43], v[210:211]
	v_pk_mul_f32 v[208:209], v[80:81], v[208:209]
	v_pk_mul_f32 v[210:211], v[82:83], v[210:211]
	global_store_dwordx4 v10, v[208:211], s[14:15] offset:1024
	s_waitcnt vmcnt(47)
	v_pk_mul_f32 v[212:213], v[42:43], v[212:213]
	v_pk_mul_f32 v[214:215], v[42:43], v[214:215]
	v_pk_mul_f32 v[212:213], v[84:85], v[212:213]
	v_pk_mul_f32 v[214:215], v[86:87], v[214:215]
	global_store_dwordx4 v10, v[212:215], s[14:15] offset:2048
	s_waitcnt vmcnt(47)
	v_pk_mul_f32 v[216:217], v[42:43], v[216:217]
	v_pk_mul_f32 v[218:219], v[42:43], v[218:219]
	v_pk_mul_f32 v[216:217], v[88:89], v[216:217]
	v_pk_mul_f32 v[218:219], v[90:91], v[218:219]
	global_store_dwordx4 v10, v[216:219], s[14:15] offset:3072
	s_waitcnt vmcnt(47)
	v_pk_mul_f32 v[220:221], v[42:43], v[220:221]
	v_pk_mul_f32 v[222:223], v[42:43], v[222:223]
	v_pk_mul_f32 v[220:221], v[92:93], v[220:221]
	v_pk_mul_f32 v[222:223], v[94:95], v[222:223]
	global_store_dwordx4 v11, v[220:223], s[14:15] offset:0
	s_waitcnt vmcnt(47)
; __device__ __forceinline__ void p12_peer(Frame& F) {
;     ...
; #pragma unroll
;               for (int c = c0; c < c0 + 8; ++c) { const size_t col = (size_t)t * D_ + (size_t)(unsigned)(256 * c + lo2_); const f32x4 gn = *(const f32x4*)(lnf + (256 * c + lo2_));
;                   const f32x4 o = *(const f32x4*)(F.out + col);
;                   *(f32x4*)(F.out + col) = (f32x4){o.x * rs * gn.x, o.y * rs * gn.y, o.z * rs * gn.z, o.w * rs * gn.w}; }
	v_pk_mul_f32 v[224:225], v[42:43], v[224:225]
	v_pk_mul_f32 v[226:227], v[42:43], v[226:227]
	v_pk_mul_f32 v[224:225], v[96:97], v[224:225]
	v_pk_mul_f32 v[226:227], v[98:99], v[226:227]
	global_store_dwordx4 v11, v[224:227], s[14:15] offset:1024
	s_waitcnt vmcnt(47)
	v_pk_mul_f32 v[228:229], v[42:43], v[228:229]
	v_pk_mul_f32 v[230:231], v[42:43], v[230:231]
	v_pk_mul_f32 v[228:229], v[100:101], v[228:229]
	v_pk_mul_f32 v[230:231], v[102:103], v[230:231]
	global_store_dwordx4 v11, v[228:231], s[14:15] offset:2048
	s_waitcnt vmcnt(47)
	v_pk_mul_f32 v[232:233], v[42:43], v[232:233]
	v_pk_mul_f32 v[234:235], v[42:43], v[234:235]
	v_pk_mul_f32 v[232:233], v[104:105], v[232:233]
	v_pk_mul_f32 v[234:235], v[106:107], v[234:235]
	global_store_dwordx4 v11, v[232:235], s[14:15] offset:3072
	s_waitcnt vmcnt(47)
	v_pk_mul_f32 v[236:237], v[42:43], v[236:237]
	v_pk_mul_f32 v[238:239], v[42:43], v[238:239]
	v_pk_mul_f32 v[236:237], v[108:109], v[236:237]
	v_pk_mul_f32 v[238:239], v[110:111], v[238:239]
	global_store_dwordx4 v12, v[236:239], s[14:15] offset:0
	s_waitcnt vmcnt(47)
	v_pk_mul_f32 v[240:241], v[42:43], v[240:241]
	v_pk_mul_f32 v[242:243], v[42:43], v[242:243]
	v_pk_mul_f32 v[240:241], v[112:113], v[240:241]
	v_pk_mul_f32 v[242:243], v[114:115], v[242:243]
	global_store_dwordx4 v12, v[240:243], s[14:15] offset:1024
	s_waitcnt vmcnt(47)
	v_pk_mul_f32 v[244:245], v[42:43], v[244:245]
	v_pk_mul_f32 v[246:247], v[42:43], v[246:247]
	v_pk_mul_f32 v[244:245], v[116:117], v[244:245]
	v_pk_mul_f32 v[246:247], v[118:119], v[246:247]
	global_store_dwordx4 v12, v[244:247], s[14:15] offset:2048
	s_waitcnt vmcnt(47)
	v_pk_mul_f32 v[248:249], v[42:43], v[248:249]
	v_pk_mul_f32 v[250:251], v[42:43], v[250:251]
	v_pk_mul_f32 v[248:249], v[120:121], v[248:249]
	v_pk_mul_f32 v[250:251], v[122:123], v[250:251]
	global_store_dwordx4 v12, v[248:251], s[14:15] offset:3072
	s_nop 1
	global_load_dwordx4 v[188:191], v6, s[18:19] offset:0
	global_load_dwordx4 v[192:195], v6, s[18:19] offset:1024
	global_load_dwordx4 v[196:199], v6, s[18:19] offset:2048
	global_load_dwordx4 v[200:203], v6, s[18:19] offset:3072
	global_load_dwordx4 v[204:207], v10, s[18:19] offset:0
	global_load_dwordx4 v[208:211], v10, s[18:19] offset:1024
	global_load_dwordx4 v[212:215], v10, s[18:19] offset:2048
	global_load_dwordx4 v[216:219], v10, s[18:19] offset:3072
	global_load_dwordx4 v[220:223], v11, s[18:19] offset:0
	global_load_dwordx4 v[224:227], v11, s[18:19] offset:1024
	global_load_dwordx4 v[228:231], v11, s[18:19] offset:2048
	global_load_dwordx4 v[232:235], v11, s[18:19] offset:3072
	global_load_dwordx4 v[236:239], v12, s[18:19] offset:0
	global_load_dwordx4 v[240:243], v12, s[18:19] offset:1024
	global_load_dwordx4 v[244:247], v12, s[18:19] offset:2048
	global_load_dwordx4 v[248:251], v12, s[18:19] offset:3072
	s_waitcnt vmcnt(47)
	v_pk_mul_f32 v[124:125], v[44:45], v[124:125]
	v_pk_mul_f32 v[126:127], v[44:45], v[126:127]
	v_pk_mul_f32 v[124:125], v[60:61], v[124:125]
	v_pk_mul_f32 v[126:127], v[62:63], v[126:127]
	global_store_dwordx4 v6, v[124:127], s[16:17] offset:0
	s_waitcnt vmcnt(47)
	v_pk_mul_f32 v[128:129], v[44:45], v[128:129]
	v_pk_mul_f32 v[130:131], v[44:45], v[130:131]
	v_pk_mul_f32 v[128:129], v[64:65], v[128:129]
	v_pk_mul_f32 v[130:131], v[66:67], v[130:131]
	global_store_dwordx4 v6, v[128:131], s[16:17] offset:1024
	s_waitcnt vmcnt(47)
	v_pk_mul_f32 v[132:133], v[44:45], v[132:133]
	v_pk_mul_f32 v[134:135], v[44:45], v[134:135]
	v_pk_mul_f32 v[132:133], v[68:69], v[132:133]
	v_pk_mul_f32 v[134:135], v[70:71], v[134:135]
	global_store_dwordx4 v6, v[132:135], s[16:17] offset:2048
	s_waitcnt vmcnt(47)
	v_pk_mul_f32 v[136:137], v[44:45], v[136:137]
	v_pk_mul_f32 v[138:139], v[44:45], v[138:139]
	v_pk_mul_f32 v[136:137], v[72:73], v[136:137]
	v_pk_mul_f32 v[138:139], v[74:75], v[138:139]
	global_store_dwordx4 v6, v[136:139], s[16:17] offset:3072
	s_waitcnt vmcnt(47)
	v_pk_mul_f32 v[140:141], v[44:45], v[140:141]
	v_pk_mul_f32 v[142:143], v[44:45], v[142:143]
	v_pk_mul_f32 v[140:141], v[76:77], v[140:141]
	v_pk_mul_f32 v[142:143], v[78:79], v[142:143]
	global_store_dwordx4 v10, v[140:143], s[16:17] offset:0
	s_waitcnt vmcnt(47)
	v_pk_mul_f32 v[144:145], v[44:45], v[144:145]
	v_pk_mul_f32 v[146:147], v[44:45], v[146:147]
	v_pk_mul_f32 v[144:145], v[80:81], v[144:145]
	v_pk_mul_f32 v[146:147], v[82:83], v[146:147]
	global_store_dwordx4 v10, v[144:147], s[16:17] offset:1024
	s_waitcnt vmcnt(47)
	v_pk_mul_f32 v[148:149], v[44:45], v[148:149]
	v_pk_mul_f32 v[150:151], v[44:45], v[150:151]
	v_pk_mul_f32 v[148:149], v[84:85], v[148:149]
	v_pk_mul_f32 v[150:151], v[86:87], v[150:151]
	global_store_dwordx4 v10, v[148:151], s[16:17] offset:2048
	s_waitcnt vmcnt(47)
	v_pk_mul_f32 v[152:153], v[44:45], v[152:153]
	v_pk_mul_f32 v[154:155], v[44:45], v[154:155]
	v_pk_mul_f32 v[152:153], v[88:89], v[152:153]
	v_pk_mul_f32 v[154:155], v[90:91], v[154:155]
	global_store_dwordx4 v10, v[152:155], s[16:17] offset:3072
	s_waitcnt vmcnt(47)
	v_pk_mul_f32 v[156:157], v[44:45], v[156:157]
	v_pk_mul_f32 v[158:159], v[44:45], v[158:159]
	v_pk_mul_f32 v[156:157], v[92:93], v[156:157]
	v_pk_mul_f32 v[158:159], v[94:95], v[158:159]
	global_store_dwordx4 v11, v[156:159], s[16:17] offset:0
	s_waitcnt vmcnt(47)
	v_pk_mul_f32 v[160:161], v[44:45], v[160:161]
	v_pk_mul_f32 v[162:163], v[44:45], v[162:163]
	v_pk_mul_f32 v[160:161], v[96:97], v[160:161]
	v_pk_mul_f32 v[162:163], v[98:99], v[162:163]
	global_store_dwordx4 v11, v[160:163], s[16:17] offset:1024
	s_waitcnt vmcnt(47)
; __device__ __forceinline__ void p12_peer(Frame& F) {
;     ...
; #pragma unroll
;               for (int c = c0; c < c0 + 8; ++c) { const size_t col = (size_t)t * D_ + (size_t)(unsigned)(256 * c + lo2_); const f32x4 gn = *(const f32x4*)(lnf + (256 * c + lo2_));
;                   const f32x4 o = *(const f32x4*)(F.out + col);
;                   *(f32x4*)(F.out + col) = (f32x4){o.x * rs * gn.x, o.y * rs * gn.y, o.z * rs * gn.z, o.w * rs * gn.w}; }
	v_pk_mul_f32 v[164:165], v[44:45], v[164:165]
	v_pk_mul_f32 v[166:167], v[44:45], v[166:167]
	v_pk_mul_f32 v[164:165], v[100:101], v[164:165]
	v_pk_mul_f32 v[166:167], v[102:103], v[166:167]
	global_store_dwordx4 v11, v[164:167], s[16:17] offset:2048
	s_waitcnt vmcnt(47)
	v_pk_mul_f32 v[168:169], v[44:45], v[168:169]
	v_pk_mul_f32 v[170:171], v[44:45], v[170:171]
	v_pk_mul_f32 v[168:169], v[104:105], v[168:169]
	v_pk_mul_f32 v[170:171], v[106:107], v[170:171]
	global_store_dwordx4 v11, v[168:171], s[16:17] offset:3072
	s_waitcnt vmcnt(47)
	v_pk_mul_f32 v[172:173], v[44:45], v[172:173]
	v_pk_mul_f32 v[174:175], v[44:45], v[174:175]
	v_pk_mul_f32 v[172:173], v[108:109], v[172:173]
	v_pk_mul_f32 v[174:175], v[110:111], v[174:175]
	global_store_dwordx4 v12, v[172:175], s[16:17] offset:0
	s_waitcnt vmcnt(47)
	v_pk_mul_f32 v[176:177], v[44:45], v[176:177]
	v_pk_mul_f32 v[178:179], v[44:45], v[178:179]
	v_pk_mul_f32 v[176:177], v[112:113], v[176:177]
	v_pk_mul_f32 v[178:179], v[114:115], v[178:179]
	global_store_dwordx4 v12, v[176:179], s[16:17] offset:1024
	s_waitcnt vmcnt(47)
	v_pk_mul_f32 v[180:181], v[44:45], v[180:181]
	v_pk_mul_f32 v[182:183], v[44:45], v[182:183]
	v_pk_mul_f32 v[180:181], v[116:117], v[180:181]
	v_pk_mul_f32 v[182:183], v[118:119], v[182:183]
	global_store_dwordx4 v12, v[180:183], s[16:17] offset:2048
	s_waitcnt vmcnt(47)
	v_pk_mul_f32 v[184:185], v[44:45], v[184:185]
	v_pk_mul_f32 v[186:187], v[44:45], v[186:187]
	v_pk_mul_f32 v[184:185], v[120:121], v[184:185]
	v_pk_mul_f32 v[186:187], v[122:123], v[186:187]
	global_store_dwordx4 v12, v[184:187], s[16:17] offset:3072
	s_waitcnt vmcnt(31)
	v_pk_mul_f32 v[188:189], v[46:47], v[188:189]
	v_pk_mul_f32 v[190:191], v[46:47], v[190:191]
	v_pk_mul_f32 v[188:189], v[60:61], v[188:189]
	v_pk_mul_f32 v[190:191], v[62:63], v[190:191]
	global_store_dwordx4 v6, v[188:191], s[18:19] offset:0
	s_waitcnt vmcnt(31)
	v_pk_mul_f32 v[192:193], v[46:47], v[192:193]
	v_pk_mul_f32 v[194:195], v[46:47], v[194:195]
	v_pk_mul_f32 v[192:193], v[64:65], v[192:193]
	v_pk_mul_f32 v[194:195], v[66:67], v[194:195]
	global_store_dwordx4 v6, v[192:195], s[18:19] offset:1024
	s_waitcnt vmcnt(31)
	v_pk_mul_f32 v[196:197], v[46:47], v[196:197]
	v_pk_mul_f32 v[198:199], v[46:47], v[198:199]
	v_pk_mul_f32 v[196:197], v[68:69], v[196:197]
	v_pk_mul_f32 v[198:199], v[70:71], v[198:199]
	global_store_dwordx4 v6, v[196:199], s[18:19] offset:2048
	s_waitcnt vmcnt(31)
	v_pk_mul_f32 v[200:201], v[46:47], v[200:201]
	v_pk_mul_f32 v[202:203], v[46:47], v[202:203]
	v_pk_mul_f32 v[200:201], v[72:73], v[200:201]
	v_pk_mul_f32 v[202:203], v[74:75], v[202:203]
	global_store_dwordx4 v6, v[200:203], s[18:19] offset:3072
	s_waitcnt vmcnt(31)
	v_pk_mul_f32 v[204:205], v[46:47], v[204:205]
	v_pk_mul_f32 v[206:207], v[46:47], v[206:207]
	v_pk_mul_f32 v[204:205], v[76:77], v[204:205]
	v_pk_mul_f32 v[206:207], v[78:79], v[206:207]
	global_store_dwordx4 v10, v[204:207], s[18:19] offset:0
	s_waitcnt vmcnt(31)
	v_pk_mul_f32 v[208:209], v[46:47], v[208:209]
	v_pk_mul_f32 v[210:211], v[46:47], v[210:211]
	v_pk_mul_f32 v[208:209], v[80:81], v[208:209]
	v_pk_mul_f32 v[210:211], v[82:83], v[210:211]
	global_store_dwordx4 v10, v[208:211], s[18:19] offset:1024
	s_waitcnt vmcnt(31)
	v_pk_mul_f32 v[212:213], v[46:47], v[212:213]
	v_pk_mul_f32 v[214:215], v[46:47], v[214:215]
	v_pk_mul_f32 v[212:213], v[84:85], v[212:213]
	v_pk_mul_f32 v[214:215], v[86:87], v[214:215]
	global_store_dwordx4 v10, v[212:215], s[18:19] offset:2048
	s_waitcnt vmcnt(31)
	v_pk_mul_f32 v[216:217], v[46:47], v[216:217]
	v_pk_mul_f32 v[218:219], v[46:47], v[218:219]
	v_pk_mul_f32 v[216:217], v[88:89], v[216:217]
	v_pk_mul_f32 v[218:219], v[90:91], v[218:219]
	global_store_dwordx4 v10, v[216:219], s[18:19] offset:3072
	s_waitcnt vmcnt(31)
	v_pk_mul_f32 v[220:221], v[46:47], v[220:221]
	v_pk_mul_f32 v[222:223], v[46:47], v[222:223]
	v_pk_mul_f32 v[220:221], v[92:93], v[220:221]
	v_pk_mul_f32 v[222:223], v[94:95], v[222:223]
	global_store_dwordx4 v11, v[220:223], s[18:19] offset:0
	s_waitcnt vmcnt(31)
	v_pk_mul_f32 v[224:225], v[46:47], v[224:225]
	v_pk_mul_f32 v[226:227], v[46:47], v[226:227]
	v_pk_mul_f32 v[224:225], v[96:97], v[224:225]
	v_pk_mul_f32 v[226:227], v[98:99], v[226:227]
	global_store_dwordx4 v11, v[224:227], s[18:19] offset:1024
	s_waitcnt vmcnt(31)
	v_pk_mul_f32 v[228:229], v[46:47], v[228:229]
	v_pk_mul_f32 v[230:231], v[46:47], v[230:231]
	v_pk_mul_f32 v[228:229], v[100:101], v[228:229]
	v_pk_mul_f32 v[230:231], v[102:103], v[230:231]
	global_store_dwordx4 v11, v[228:231], s[18:19] offset:2048
	s_waitcnt vmcnt(31)
	v_pk_mul_f32 v[232:233], v[46:47], v[232:233]
	v_pk_mul_f32 v[234:235], v[46:47], v[234:235]
	v_pk_mul_f32 v[232:233], v[104:105], v[232:233]
	v_pk_mul_f32 v[234:235], v[106:107], v[234:235]
	global_store_dwordx4 v11, v[232:235], s[18:19] offset:3072
	s_waitcnt vmcnt(31)
	v_pk_mul_f32 v[236:237], v[46:47], v[236:237]
	v_pk_mul_f32 v[238:239], v[46:47], v[238:239]
	v_pk_mul_f32 v[236:237], v[108:109], v[236:237]
	v_pk_mul_f32 v[238:239], v[110:111], v[238:239]
	global_store_dwordx4 v12, v[236:239], s[18:19] offset:0
	s_waitcnt vmcnt(31)
	v_pk_mul_f32 v[240:241], v[46:47], v[240:241]
	v_pk_mul_f32 v[242:243], v[46:47], v[242:243]
	v_pk_mul_f32 v[240:241], v[112:113], v[240:241]
	v_pk_mul_f32 v[242:243], v[114:115], v[242:243]
	global_store_dwordx4 v12, v[240:243], s[18:19] offset:1024
	s_waitcnt vmcnt(31)
	v_pk_mul_f32 v[244:245], v[46:47], v[244:245]
	v_pk_mul_f32 v[246:247], v[46:47], v[246:247]
	v_pk_mul_f32 v[244:245], v[116:117], v[244:245]
	v_pk_mul_f32 v[246:247], v[118:119], v[246:247]
	global_store_dwordx4 v12, v[244:247], s[18:19] offset:2048
	s_waitcnt vmcnt(31)
	v_pk_mul_f32 v[248:249], v[46:47], v[248:249]
	v_pk_mul_f32 v[250:251], v[46:47], v[250:251]
	v_pk_mul_f32 v[248:249], v[120:121], v[248:249]
	v_pk_mul_f32 v[250:251], v[122:123], v[250:251]
	global_store_dwordx4 v12, v[248:251], s[18:19] offset:3072
